# w_in1/w_out1/part of moe13 int8 weight conversion moved from the prologue to idle workgroups in the w_out GEMM tail rounds (2 tasks per idle CU)
# speedup vs baseline: 1.0065x; 1.0065x over previous
.LBB0_109:
	v_readlane_b32 s0, v251, 5
	v_readlane_b32 s6, v251, 11
	v_readlane_b32 s7, v251, 12
	s_add_u32 s0, s6, 0x10f00000
	v_writelane_b32 v252, s0, 12
	s_addc_u32 s0, s7, 0
	v_writelane_b32 v252, s0, 13
	s_add_u32 s0, s6, 0x3c90c0
	v_writelane_b32 v252, s0, 14
	s_addc_u32 s0, s7, 0
	v_writelane_b32 v252, s0, 15
	s_add_u32 s0, s6, 0x3ad0c0
	v_writelane_b32 v252, s0, 16
	s_addc_u32 s0, s7, 0
	v_writelane_b32 v252, s0, 17
	s_add_u32 s0, s6, 0x13800000
	v_writelane_b32 v252, s0, 18
	s_addc_u32 s0, s7, 0
	v_writelane_b32 v252, s0, 19
	s_add_u32 s0, s6, 0x33d0c0
	v_writelane_b32 v252, s0, 20
	s_addc_u32 s0, s7, 0
	v_writelane_b32 v252, s0, 21
	s_add_u32 s0, s6, 0x11700000
	v_writelane_b32 v252, s0, 22
	s_addc_u32 s0, s7, 0
	v_writelane_b32 v252, s0, 23
	s_add_u32 s0, s6, 0x3320c0
	v_mov_b32_e32 v0, 0x135f
	v_readlane_b32 s1, v251, 6
	v_writelane_b32 v252, s0, 24
	s_addc_u32 s0, s7, 0
	v_cmp_gt_i32_e32 vcc, s28, v0
	v_readlane_b32 s2, v251, 7
	v_readlane_b32 s3, v251, 8
	v_readlane_b32 s4, v251, 9
	v_readlane_b32 s5, v251, 10
	v_writelane_b32 v252, s0, 25
	s_and_b64 s[0:1], vcc, exec
	s_mov_b64 s[0:1], s[52:53]
	s_mov_b64 s[2:3], s[54:55]
	s_mov_b64 s[4:5], s[56:57]
	s_mov_b64 s[6:7], s[58:59]
	s_mov_b64 s[8:9], s[60:61]
	s_mov_b64 s[10:11], s[62:63]
	s_mov_b64 s[12:13], s[64:65]
	v_writelane_b32 v252, s0, 26
	s_waitcnt lgkmcnt(0)
	s_barrier
	v_writelane_b32 v252, s1, 27
	v_writelane_b32 v252, s2, 28
	v_writelane_b32 v252, s3, 29
	v_writelane_b32 v252, s4, 30
	v_writelane_b32 v252, s5, 31
	v_writelane_b32 v252, s6, 32
	v_writelane_b32 v252, s7, 33
	v_writelane_b32 v252, s8, 34
	v_writelane_b32 v252, s9, 35
	v_writelane_b32 v252, s10, 36
	v_writelane_b32 v252, s11, 37
	v_writelane_b32 v252, s12, 38
	v_writelane_b32 v252, s13, 39
	v_writelane_b32 v252, s14, 40
	v_writelane_b32 v252, s15, 41
	s_cbranch_scc1 .LBB0_253
	s_mov_b32 s98, s28
	v_readlane_b32 s100, v251, 24
	s_movk_i32 s99, 0xdc0
	s_mov_b32 s101, 0
	s_mov_b32 s0, 0xfffff530
	s_cmp_lt_u32 s98, 0x1330
	s_cselect_b32 s0, 0x30, s0
	s_cmp_lt_u32 s98, 0x1310
	s_cselect_b32 s0, 0xffffffd0, s0
	s_cmp_lt_u32 s98, 0x1230
	s_cselect_b32 s0, 0xffffef30, s0
	s_cmp_lt_u32 s98, 0x1180
	s_cselect_b32 s0, 0xfffff2a0, s0
	s_cmp_lt_u32 s98, 0xfa0
	s_cselect_b32 s0, 0xfffff2a0, s0
	s_cmp_lt_u32 s98, 0xec0
	s_cselect_b32 s0, 0x460, s0
	s_cmp_lt_u32 s98, 0xea0
	s_cselect_b32 s0, 0x280, s0
	s_cmp_lt_u32 s98, 0xdc0
	s_cselect_b32 s0, 0x1a0, s0
	s_cmp_lt_u32 s98, 0x6f0
	s_cselect_b32 s0, 0xc50, s0
	s_cmp_lt_u32 s98, 0x6d0
	s_cselect_b32 s0, 0xb30, s0
	s_cmp_lt_u32 s98, 0x5f0
	s_cselect_b32 s0, 0x270, s0
	s_cmp_lt_u32 s98, 0x1b0
	s_cselect_b32 s0, 0x1150, s0
	s_cmp_lt_u32 s98, 0x190
	s_cselect_b32 s0, 0xeb0, s0
	s_cmp_lt_u32 s98, 0xb0
	s_cselect_b32 s0, 0x0, s0
	s_add_i32 s28, s98, s0
	v_lshlrev_b32_e32 v0, 2, v50
	s_add_i32 s0, 0, 0x21000
	v_and_b32_e32 v37, 31, v50
	v_add_u32_e32 v39, s0, v0
	v_cmp_gt_i32_e64 s[0:1], 32, v50
	v_lshlrev_b32_e32 v1, 1, v50
	v_lshlrev_b32_e32 v42, 2, v37
	v_writelane_b32 v252, s0, 42
	v_ashrrev_i32_e32 v40, 3, v50
	v_and_b32_e32 v2, 0xffffffc0, v1
	v_add_u32_e32 v4, 0, v42
	v_writelane_b32 v252, s1, 43
	s_add_i32 s0, 0, 0x21800
	s_movk_i32 s2, 0x84
	v_and_b32_e32 v45, 7, v50
	v_add_u32_e32 v43, s0, v0
	v_add_u32_e32 v82, s0, v42
	v_mad_u64_u32 v[6:7], s[0:1], v2, s2, v[4:5]
	v_mul_lo_u32 v41, v40, s2
	v_lshlrev_b32_e32 v45, 4, v45
	v_add3_u32 v83, v41, v45, 0
	v_lshrrev_b32_e32 v45, 5, v50
	s_movk_i32 s0, 0x2100
	v_and_b32_e32 v35, 28, v0
	v_or_b32_e32 v0, 62, v1
	v_or_b32_e32 v1, 63, v1
	v_mul_lo_u32 v84, v45, s0
	v_mul_lo_u32 v0, v0, s2
	v_mul_lo_u32 v44, v1, s2
	v_or_b32_e32 v10, 2, v2
	v_or_b32_e32 v12, 4, v2
	v_or_b32_e32 v14, 6, v2
	v_or_b32_e32 v16, 8, v2
	v_or_b32_e32 v18, 10, v2
	v_or_b32_e32 v20, 12, v2
	v_or_b32_e32 v22, 14, v2
	v_or_b32_e32 v24, 16, v2
	v_or_b32_e32 v26, 18, v2
	v_or_b32_e32 v28, 20, v2
	v_or_b32_e32 v30, 22, v2
	v_or_b32_e32 v32, 24, v2
	v_or_b32_e32 v34, 26, v2
	v_or_b32_e32 v36, 28, v2
	v_or_b32_e32 v38, 30, v2
	v_ashrrev_i32_e32 v41, 31, v40
	v_or_b32_e32 v42, v84, v42
	v_ashrrev_i32_e32 v3, 31, v2
	v_mov_b32_e32 v8, v2
	v_mov_b32_e32 v1, v2
	v_mov_b32_e32 v5, v10
	v_mov_b32_e32 v7, v12
	v_mov_b32_e32 v9, v14
	v_mov_b32_e32 v11, v16
	v_mov_b32_e32 v13, v18
	v_mov_b32_e32 v15, v20
	v_mov_b32_e32 v17, v22
	v_mov_b32_e32 v19, v24
	v_mov_b32_e32 v21, v26
	v_mov_b32_e32 v23, v28
	v_mov_b32_e32 v25, v30
	v_mov_b32_e32 v27, v32
	v_mov_b32_e32 v29, v34
	v_mov_b32_e32 v31, v36
	v_mov_b32_e32 v33, v38
	v_lshlrev_b64 v[40:41], 2, v[40:41]
	v_add_u32_e32 v42, 0, v42
	v_mov_b32_e32 v45, 0
	v_add_u32_e32 v85, v4, v0
	v_add_u32_e32 v86, v4, v44
	s_branch .LBB0_112
.LBB0_111:
	s_or_b64 exec, exec, s[0:1]
	s_waitcnt lgkmcnt(0)
	s_barrier
	ds_read_b32 v0, v82
	ds_read_b32 v44, v85
	ds_read_b32 v58, v86
	s_mov_b32 s2, 0x42fe0000
	v_add_u32_e32 v57, 0x400, v6
	s_waitcnt lgkmcnt(2)
	v_div_scale_f32 v46, s[0:1], v0, v0, s2
	v_rcp_f32_e32 v47, v46
	v_readlane_b32 s0, v252, 46
	v_readlane_b32 s1, v252, 47
	v_add_u32_e32 v60, 0x800, v6
	v_fma_f32 v48, -v46, v47, 1.0
	v_fmac_f32_e32 v47, v48, v47
	v_div_scale_f32 v48, vcc, s2, v0, s2
	v_mul_f32_e32 v49, v48, v47
	v_fma_f32 v52, -v46, v49, v48
	v_fmac_f32_e32 v49, v52, v47
	v_fma_f32 v46, -v46, v49, v48
	v_div_fmas_f32 v46, v46, v47, v49
	ds_read2_b32 v[48:49], v6 offset1:33
	v_div_fixup_f32 v46, v46, v0, s2
	v_cmp_lt_f32_e32 vcc, 0, v0
	ds_read2_b32 v[52:53], v6 offset0:66 offset1:99
	v_readlane_b32 s28, v252, 44
	v_cndmask_b32_e32 v0, 0, v46, vcc
	s_waitcnt lgkmcnt(1)
	v_mul_f32_e32 v48, v48, v0
	v_rndne_f32_e32 v48, v48
	v_cvt_i32_f32_e32 v54, v48
	v_mul_f32_e32 v48, v0, v49
	v_rndne_f32_e32 v48, v48
	v_cvt_i32_f32_e32 v55, v48
	s_waitcnt lgkmcnt(0)
	v_mul_f32_e32 v48, v0, v52
	v_rndne_f32_e32 v48, v48
	v_cvt_i32_f32_sdwa v52, v48 dst_sel:WORD_1 dst_unused:UNUSED_PAD src0_sel:DWORD
	v_mul_f32_e32 v48, v0, v53
	v_or_b32_e32 v46, s33, v37
	v_rndne_f32_e32 v48, v48
	v_ashrrev_i32_e32 v47, 31, v46
	v_cvt_i32_f32_sdwa v53, v48 dst_sel:BYTE_3 dst_unused:UNUSED_PAD src0_sel:DWORD
	ds_read2_b32 v[48:49], v6 offset0:132 offset1:165
	v_lshlrev_b64 v[46:47], 10, v[46:47]
	v_lshl_add_u64 v[46:47], s[0:1], 0, v[46:47]
	v_lshlrev_b32_e32 v55, 8, v55
	s_mov_b32 s0, 0xc0c0500
	v_perm_b32 v54, v55, v54, s0
	v_and_b32_e32 v52, 0xff0000, v52
	v_or3_b32 v52, v54, v52, v53
	ds_read2_b32 v[54:55], v6 offset0:198 offset1:231
	s_waitcnt lgkmcnt(1)
	v_mul_f32_e32 v48, v0, v48
	v_rndne_f32_e32 v48, v48
	v_cvt_i32_f32_e32 v53, v48
	v_mul_f32_e32 v48, v0, v49
	v_rndne_f32_e32 v48, v48
	v_cvt_i32_f32_e32 v56, v48
	s_waitcnt lgkmcnt(0)
	v_mul_f32_e32 v48, v0, v54
	v_rndne_f32_e32 v48, v48
	v_cvt_i32_f32_sdwa v54, v48 dst_sel:WORD_1 dst_unused:UNUSED_PAD src0_sel:DWORD
	v_mul_f32_e32 v48, v0, v55
	v_rndne_f32_e32 v48, v48
	v_cvt_i32_f32_sdwa v55, v48 dst_sel:BYTE_3 dst_unused:UNUSED_PAD src0_sel:DWORD
	ds_read2_b32 v[48:49], v57 offset0:8 offset1:41
	v_lshlrev_b32_e32 v56, 8, v56
	v_perm_b32 v53, v56, v53, s0
	v_and_b32_e32 v54, 0xff0000, v54
	v_or3_b32 v53, v53, v54, v55
	ds_read2_b32 v[54:55], v57 offset0:74 offset1:107
	s_waitcnt lgkmcnt(1)
	v_mul_f32_e32 v48, v0, v48
	v_rndne_f32_e32 v48, v48
	v_cvt_i32_f32_e32 v56, v48
	v_mul_f32_e32 v48, v0, v49
	v_rndne_f32_e32 v48, v48
	v_cvt_i32_f32_e32 v59, v48
	s_waitcnt lgkmcnt(0)
	v_mul_f32_e32 v48, v0, v54
	v_rndne_f32_e32 v48, v48
	v_cvt_i32_f32_sdwa v54, v48 dst_sel:WORD_1 dst_unused:UNUSED_PAD src0_sel:DWORD
	v_mul_f32_e32 v48, v0, v55
	v_rndne_f32_e32 v48, v48
	v_cvt_i32_f32_sdwa v55, v48 dst_sel:BYTE_3 dst_unused:UNUSED_PAD src0_sel:DWORD
	ds_read2_b32 v[48:49], v57 offset0:140 offset1:173
	v_lshlrev_b32_e32 v59, 8, v59
	v_perm_b32 v56, v59, v56, s0
	v_and_b32_e32 v54, 0xff0000, v54
	v_or3_b32 v54, v56, v54, v55
	ds_read2_b32 v[56:57], v57 offset0:206 offset1:239
	s_waitcnt lgkmcnt(1)
	v_mul_f32_e32 v48, v0, v48
	v_mul_f32_e32 v49, v0, v49
	v_rndne_f32_e32 v48, v48
	v_rndne_f32_e32 v49, v49
	v_cvt_i32_f32_e32 v55, v48
	s_waitcnt lgkmcnt(0)
	v_mul_f32_e32 v48, v0, v56
	v_cvt_i32_f32_e32 v49, v49
	v_rndne_f32_e32 v48, v48
	v_cvt_i32_f32_sdwa v56, v48 dst_sel:WORD_1 dst_unused:UNUSED_PAD src0_sel:DWORD
	v_mul_f32_e32 v48, v0, v57
	v_rndne_f32_e32 v48, v48
	v_cvt_i32_f32_sdwa v57, v48 dst_sel:BYTE_3 dst_unused:UNUSED_PAD src0_sel:DWORD
	v_lshlrev_b32_e32 v59, 8, v49
	ds_read2_b32 v[48:49], v60 offset0:16 offset1:49
	v_perm_b32 v55, v59, v55, s0
	v_and_b32_e32 v56, 0xff0000, v56
	v_lshl_add_u64 v[46:47], v[46:47], 0, v[2:3]
	v_or3_b32 v55, v55, v56, v57
	global_store_dwordx4 v[46:47], v[52:55], off
	ds_read2_b32 v[52:53], v60 offset0:82 offset1:115
	s_waitcnt lgkmcnt(1)
	v_mul_f32_e32 v48, v0, v48
	v_rndne_f32_e32 v48, v48
	v_cvt_i32_f32_e32 v54, v48
	v_mul_f32_e32 v48, v0, v49
	v_rndne_f32_e32 v48, v48
	v_cvt_i32_f32_e32 v55, v48
	s_waitcnt lgkmcnt(0)
	v_mul_f32_e32 v48, v0, v52
	v_rndne_f32_e32 v48, v48
	v_cvt_i32_f32_sdwa v52, v48 dst_sel:WORD_1 dst_unused:UNUSED_PAD src0_sel:DWORD
	v_mul_f32_e32 v48, v0, v53
	v_rndne_f32_e32 v48, v48
	v_cvt_i32_f32_sdwa v53, v48 dst_sel:BYTE_3 dst_unused:UNUSED_PAD src0_sel:DWORD
	ds_read2_b32 v[48:49], v60 offset0:148 offset1:181
	v_lshlrev_b32_e32 v55, 8, v55
	v_perm_b32 v54, v55, v54, s0
	v_and_b32_e32 v52, 0xff0000, v52
	v_or3_b32 v52, v54, v52, v53
	ds_read2_b32 v[54:55], v60 offset0:214 offset1:247
	s_waitcnt lgkmcnt(1)
	v_mul_f32_e32 v48, v0, v48
	v_rndne_f32_e32 v48, v48
	v_cvt_i32_f32_e32 v53, v48
	v_mul_f32_e32 v48, v0, v49
	v_rndne_f32_e32 v48, v48
	v_cvt_i32_f32_e32 v56, v48
	s_waitcnt lgkmcnt(0)
	v_mul_f32_e32 v48, v0, v54
	v_rndne_f32_e32 v48, v48
	v_cvt_i32_f32_sdwa v54, v48 dst_sel:WORD_1 dst_unused:UNUSED_PAD src0_sel:DWORD
	v_mul_f32_e32 v48, v0, v55
	v_rndne_f32_e32 v48, v48
	v_add_u32_e32 v57, 0xc00, v6
	v_cvt_i32_f32_sdwa v55, v48 dst_sel:BYTE_3 dst_unused:UNUSED_PAD src0_sel:DWORD
	ds_read2_b32 v[48:49], v57 offset0:24 offset1:57
	v_lshlrev_b32_e32 v56, 8, v56
	v_perm_b32 v53, v56, v53, s0
	v_and_b32_e32 v54, 0xff0000, v54
	v_or3_b32 v53, v53, v54, v55
	ds_read2_b32 v[54:55], v57 offset0:90 offset1:123
	s_waitcnt lgkmcnt(1)
	v_mul_f32_e32 v48, v0, v48
	v_rndne_f32_e32 v48, v48
	v_cvt_i32_f32_e32 v56, v48
	v_mul_f32_e32 v48, v0, v49
	v_rndne_f32_e32 v48, v48
	v_cvt_i32_f32_e32 v59, v48
	s_waitcnt lgkmcnt(0)
	v_mul_f32_e32 v48, v0, v54
	v_rndne_f32_e32 v48, v48
	v_cvt_i32_f32_sdwa v54, v48 dst_sel:WORD_1 dst_unused:UNUSED_PAD src0_sel:DWORD
	v_mul_f32_e32 v48, v0, v55
	v_rndne_f32_e32 v48, v48
	v_cvt_i32_f32_sdwa v55, v48 dst_sel:BYTE_3 dst_unused:UNUSED_PAD src0_sel:DWORD
	ds_read2_b32 v[48:49], v57 offset0:156 offset1:189
	v_lshlrev_b32_e32 v59, 8, v59
	v_perm_b32 v56, v59, v56, s0
	v_and_b32_e32 v54, 0xff0000, v54
	v_or3_b32 v54, v56, v54, v55
	ds_read2_b32 v[56:57], v57 offset0:222 offset1:255
	s_waitcnt lgkmcnt(1)
	v_mul_f32_e32 v48, v0, v48
	v_mul_f32_e32 v49, v0, v49
	v_rndne_f32_e32 v48, v48
	v_rndne_f32_e32 v49, v49
	v_cvt_i32_f32_e32 v55, v48
	s_waitcnt lgkmcnt(0)
	v_mul_f32_e32 v48, v0, v56
	v_cvt_i32_f32_e32 v49, v49
	v_rndne_f32_e32 v48, v48
	v_cvt_i32_f32_sdwa v56, v48 dst_sel:WORD_1 dst_unused:UNUSED_PAD src0_sel:DWORD
	v_mul_f32_e32 v48, v0, v57
	v_rndne_f32_e32 v48, v48
	v_cvt_i32_f32_sdwa v57, v48 dst_sel:BYTE_3 dst_unused:UNUSED_PAD src0_sel:DWORD
	v_add_u32_e32 v60, 0x1000, v6
	v_lshlrev_b32_e32 v59, 8, v49
	ds_read2_b32 v[48:49], v60 offset0:32 offset1:65
	v_perm_b32 v55, v59, v55, s0
	v_and_b32_e32 v56, 0xff0000, v56
	v_or3_b32 v55, v55, v56, v57
	global_store_dwordx4 v[46:47], v[52:55], off offset:16
	ds_read2_b32 v[52:53], v60 offset0:98 offset1:131
	s_waitcnt lgkmcnt(1)
	v_mul_f32_e32 v48, v0, v48
	v_rndne_f32_e32 v48, v48
	v_cvt_i32_f32_e32 v54, v48
	v_mul_f32_e32 v48, v0, v49
	v_rndne_f32_e32 v48, v48
	v_cvt_i32_f32_e32 v55, v48
	s_waitcnt lgkmcnt(0)
	v_mul_f32_e32 v48, v0, v52
	v_rndne_f32_e32 v48, v48
	v_cvt_i32_f32_sdwa v52, v48 dst_sel:WORD_1 dst_unused:UNUSED_PAD src0_sel:DWORD
	v_mul_f32_e32 v48, v0, v53
	v_rndne_f32_e32 v48, v48
	v_cvt_i32_f32_sdwa v53, v48 dst_sel:BYTE_3 dst_unused:UNUSED_PAD src0_sel:DWORD
	ds_read2_b32 v[48:49], v60 offset0:164 offset1:197
	v_lshlrev_b32_e32 v55, 8, v55
	v_perm_b32 v54, v55, v54, s0
	v_and_b32_e32 v52, 0xff0000, v52
	v_or3_b32 v52, v54, v52, v53
	v_add_u32_e32 v53, 0x1200, v6
	ds_read2_b32 v[54:55], v53 offset0:102 offset1:135
	s_waitcnt lgkmcnt(1)
	v_mul_f32_e32 v48, v0, v48
	v_rndne_f32_e32 v48, v48
	v_cvt_i32_f32_e32 v53, v48
	v_mul_f32_e32 v48, v0, v49
	v_rndne_f32_e32 v48, v48
	v_cvt_i32_f32_e32 v56, v48
	s_waitcnt lgkmcnt(0)
	v_mul_f32_e32 v48, v0, v54
	v_rndne_f32_e32 v48, v48
	v_cvt_i32_f32_sdwa v54, v48 dst_sel:WORD_1 dst_unused:UNUSED_PAD src0_sel:DWORD
	v_mul_f32_e32 v48, v0, v55
	v_rndne_f32_e32 v48, v48
	v_add_u32_e32 v57, 0x1400, v6
	v_cvt_i32_f32_sdwa v55, v48 dst_sel:BYTE_3 dst_unused:UNUSED_PAD src0_sel:DWORD
	ds_read2_b32 v[48:49], v57 offset0:40 offset1:73
	v_lshlrev_b32_e32 v56, 8, v56
	v_perm_b32 v53, v56, v53, s0
	v_and_b32_e32 v54, 0xff0000, v54
	v_or3_b32 v53, v53, v54, v55
	ds_read2_b32 v[54:55], v57 offset0:106 offset1:139
	s_waitcnt lgkmcnt(1)
	v_mul_f32_e32 v48, v0, v48
	v_rndne_f32_e32 v48, v48
	v_cvt_i32_f32_e32 v56, v48
	v_mul_f32_e32 v48, v0, v49
	v_rndne_f32_e32 v48, v48
	v_cvt_i32_f32_e32 v59, v48
	s_waitcnt lgkmcnt(0)
	v_mul_f32_e32 v48, v0, v54
	v_rndne_f32_e32 v48, v48
	v_cvt_i32_f32_sdwa v54, v48 dst_sel:WORD_1 dst_unused:UNUSED_PAD src0_sel:DWORD
	v_mul_f32_e32 v48, v0, v55
	v_rndne_f32_e32 v48, v48
	v_cvt_i32_f32_sdwa v55, v48 dst_sel:BYTE_3 dst_unused:UNUSED_PAD src0_sel:DWORD
	ds_read2_b32 v[48:49], v57 offset0:172 offset1:205
	v_lshlrev_b32_e32 v57, 8, v59
	v_perm_b32 v56, v57, v56, s0
	v_and_b32_e32 v54, 0xff0000, v54
	v_or3_b32 v54, v56, v54, v55
	v_add_u32_e32 v55, 0x1600, v6
	ds_read2_b32 v[56:57], v55 offset0:110 offset1:143
	s_waitcnt lgkmcnt(1)
	v_mul_f32_e32 v48, v0, v48
	v_mul_f32_e32 v49, v0, v49
	v_rndne_f32_e32 v48, v48
	v_rndne_f32_e32 v49, v49
	v_cvt_i32_f32_e32 v55, v48
	s_waitcnt lgkmcnt(0)
	v_mul_f32_e32 v48, v0, v56
	v_cvt_i32_f32_e32 v49, v49
	v_rndne_f32_e32 v48, v48
	v_cvt_i32_f32_sdwa v56, v48 dst_sel:WORD_1 dst_unused:UNUSED_PAD src0_sel:DWORD
	v_mul_f32_e32 v48, v0, v57
	v_rndne_f32_e32 v48, v48
	v_cvt_i32_f32_sdwa v57, v48 dst_sel:BYTE_3 dst_unused:UNUSED_PAD src0_sel:DWORD
	v_add_u32_e32 v60, 0x1800, v6
	v_lshlrev_b32_e32 v59, 8, v49
	ds_read2_b32 v[48:49], v60 offset0:48 offset1:81
	v_perm_b32 v55, v59, v55, s0
	v_and_b32_e32 v56, 0xff0000, v56
	v_or3_b32 v55, v55, v56, v57
	global_store_dwordx4 v[46:47], v[52:55], off offset:32
	ds_read2_b32 v[52:53], v60 offset0:114 offset1:147
	s_waitcnt lgkmcnt(1)
	v_mul_f32_e32 v48, v0, v48
	v_rndne_f32_e32 v48, v48
	v_cvt_i32_f32_e32 v54, v48
	v_mul_f32_e32 v48, v0, v49
	v_rndne_f32_e32 v48, v48
	v_cvt_i32_f32_e32 v55, v48
	s_waitcnt lgkmcnt(0)
	v_mul_f32_e32 v48, v0, v52
	v_rndne_f32_e32 v48, v48
	v_cvt_i32_f32_sdwa v52, v48 dst_sel:WORD_1 dst_unused:UNUSED_PAD src0_sel:DWORD
	v_mul_f32_e32 v48, v0, v53
	v_rndne_f32_e32 v48, v48
	v_cvt_i32_f32_sdwa v53, v48 dst_sel:BYTE_3 dst_unused:UNUSED_PAD src0_sel:DWORD
	ds_read2_b32 v[48:49], v60 offset0:180 offset1:213
	v_lshlrev_b32_e32 v55, 8, v55
	v_perm_b32 v54, v55, v54, s0
	v_and_b32_e32 v52, 0xff0000, v52
	v_or3_b32 v52, v54, v52, v53
	v_add_u32_e32 v53, 0x1a00, v6
	ds_read2_b32 v[54:55], v53 offset0:118 offset1:151
	s_waitcnt lgkmcnt(1)
	v_mul_f32_e32 v48, v0, v48
	v_rndne_f32_e32 v48, v48
	v_cvt_i32_f32_e32 v53, v48
	v_mul_f32_e32 v48, v0, v49
	v_rndne_f32_e32 v48, v48
	v_cvt_i32_f32_e32 v56, v48
	s_waitcnt lgkmcnt(0)
	v_mul_f32_e32 v48, v0, v54
	v_rndne_f32_e32 v48, v48
	v_cvt_i32_f32_sdwa v54, v48 dst_sel:WORD_1 dst_unused:UNUSED_PAD src0_sel:DWORD
	v_mul_f32_e32 v48, v0, v55
	v_rndne_f32_e32 v48, v48
	v_add_u32_e32 v57, 0x1c00, v6
	v_cvt_i32_f32_sdwa v55, v48 dst_sel:BYTE_3 dst_unused:UNUSED_PAD src0_sel:DWORD
	ds_read2_b32 v[48:49], v57 offset0:56 offset1:89
	v_lshlrev_b32_e32 v56, 8, v56
	v_perm_b32 v53, v56, v53, s0
	v_and_b32_e32 v54, 0xff0000, v54
	v_or3_b32 v53, v53, v54, v55
	ds_read2_b32 v[54:55], v57 offset0:122 offset1:155
	s_waitcnt lgkmcnt(1)
	v_mul_f32_e32 v48, v0, v48
	v_rndne_f32_e32 v48, v48
	v_cvt_i32_f32_e32 v56, v48
	v_mul_f32_e32 v48, v0, v49
	v_rndne_f32_e32 v48, v48
	v_cvt_i32_f32_e32 v59, v48
	s_waitcnt lgkmcnt(0)
	v_mul_f32_e32 v48, v0, v54
	v_rndne_f32_e32 v48, v48
	v_cvt_i32_f32_sdwa v54, v48 dst_sel:WORD_1 dst_unused:UNUSED_PAD src0_sel:DWORD
	v_mul_f32_e32 v48, v0, v55
	v_rndne_f32_e32 v48, v48
	v_cvt_i32_f32_sdwa v55, v48 dst_sel:BYTE_3 dst_unused:UNUSED_PAD src0_sel:DWORD
	ds_read2_b32 v[48:49], v57 offset0:188 offset1:221
	v_mul_f32_e32 v44, v0, v44
	v_rndne_f32_e32 v44, v44
	v_cvt_i32_f32_sdwa v44, v44 dst_sel:WORD_1 dst_unused:UNUSED_PAD src0_sel:DWORD
	v_lshlrev_b32_e32 v57, 8, v59
	s_waitcnt lgkmcnt(0)
	v_mul_f32_e32 v49, v0, v49
	v_mul_f32_e32 v48, v0, v48
	v_rndne_f32_e32 v49, v49
	v_rndne_f32_e32 v48, v48
	v_cvt_i32_f32_e32 v49, v49
	v_cvt_i32_f32_e32 v48, v48
	v_mul_f32_e32 v0, v0, v58
	v_rndne_f32_e32 v0, v0
	v_cvt_i32_f32_sdwa v0, v0 dst_sel:BYTE_3 dst_unused:UNUSED_PAD src0_sel:DWORD
	v_lshlrev_b32_e32 v49, 8, v49
	v_perm_b32 v56, v57, v56, s0
	v_perm_b32 v48, v49, v48, s0
	s_add_i32 s98, s98, s100
	v_and_b32_e32 v54, 0xff0000, v54
	v_and_b32_e32 v44, 0xff0000, v44
	s_mov_b32 s0, 0xfffff530
	s_cmp_lt_u32 s98, 0x1330
	s_cselect_b32 s0, 0x30, s0
	s_cmp_lt_u32 s98, 0x1310
	s_cselect_b32 s0, 0xffffffd0, s0
	s_cmp_lt_u32 s98, 0x1230
	s_cselect_b32 s0, 0xffffef30, s0
	s_cmp_lt_u32 s98, 0x1180
	s_cselect_b32 s0, 0xfffff2a0, s0
	s_cmp_lt_u32 s98, 0xfa0
	s_cselect_b32 s0, 0xfffff2a0, s0
	s_cmp_lt_u32 s98, 0xec0
	s_cselect_b32 s0, 0x460, s0
	s_cmp_lt_u32 s98, 0xea0
	s_cselect_b32 s0, 0x280, s0
	s_cmp_lt_u32 s98, 0xdc0
	s_cselect_b32 s0, 0x1a0, s0
	s_cmp_lt_u32 s98, 0x6f0
	s_cselect_b32 s0, 0xc50, s0
	s_cmp_lt_u32 s98, 0x6d0
	s_cselect_b32 s0, 0xb30, s0
	s_cmp_lt_u32 s98, 0x5f0
	s_cselect_b32 s0, 0x270, s0
	s_cmp_lt_u32 s98, 0x1b0
	s_cselect_b32 s0, 0x1150, s0
	s_cmp_lt_u32 s98, 0x190
	s_cselect_b32 s0, 0xeb0, s0
	s_cmp_lt_u32 s98, 0xb0
	s_cselect_b32 s0, 0x0, s0
	s_add_i32 s28, s98, s0
	v_or3_b32 v54, v56, v54, v55
	v_or3_b32 v55, v48, v44, v0
	s_cmp_ge_u32 s98, s99
	global_store_dwordx4 v[46:47], v[52:55], off offset:48
	s_barrier
	s_cbranch_scc1 .LBB0_253

.Lwqd_entry:
	v_mov_b32_e32 v50, v246
	v_mov_b32_e32 v5, 0
	v_readlane_b32 s52, v252, 26
	v_readlane_b32 s53, v252, 27
	s_mov_b32 s0, 0xfffff530
	s_cmp_lt_u32 s98, 0x1330
	s_cselect_b32 s0, 0x30, s0
	s_cmp_lt_u32 s98, 0x1310
	s_cselect_b32 s0, 0xffffffd0, s0
	s_cmp_lt_u32 s98, 0x1230
	s_cselect_b32 s0, 0xffffef30, s0
	s_cmp_lt_u32 s98, 0x1180
	s_cselect_b32 s0, 0xfffff2a0, s0
	s_cmp_lt_u32 s98, 0xfa0
	s_cselect_b32 s0, 0xfffff2a0, s0
	s_cmp_lt_u32 s98, 0xec0
	s_cselect_b32 s0, 0x460, s0
	s_cmp_lt_u32 s98, 0xea0
	s_cselect_b32 s0, 0x280, s0
	s_cmp_lt_u32 s98, 0xdc0
	s_cselect_b32 s0, 0x1a0, s0
	s_cmp_lt_u32 s98, 0x6f0
	s_cselect_b32 s0, 0xc50, s0
	s_cmp_lt_u32 s98, 0x6d0
	s_cselect_b32 s0, 0xb30, s0
	s_cmp_lt_u32 s98, 0x5f0
	s_cselect_b32 s0, 0x270, s0
	s_cmp_lt_u32 s98, 0x1b0
	s_cselect_b32 s0, 0x1150, s0
	s_cmp_lt_u32 s98, 0x190
	s_cselect_b32 s0, 0xeb0, s0
	s_cmp_lt_u32 s98, 0xb0
	s_cselect_b32 s0, 0x0, s0
	s_add_i32 s28, s98, s0
	v_lshlrev_b32_e32 v0, 2, v50
	s_add_i32 s0, 0, 0x21000
	v_and_b32_e32 v37, 31, v50
	v_add_u32_e32 v39, s0, v0
	v_cmp_gt_i32_e64 s[0:1], 32, v50
	v_lshlrev_b32_e32 v1, 1, v50
	v_lshlrev_b32_e32 v42, 2, v37
	v_writelane_b32 v116, s0, 0
	v_ashrrev_i32_e32 v40, 3, v50
	v_and_b32_e32 v2, 0xffffffc0, v1
	v_add_u32_e32 v4, 0, v42
	v_writelane_b32 v116, s1, 1
	s_add_i32 s0, 0, 0x21800
	s_movk_i32 s2, 0x84
	v_and_b32_e32 v45, 7, v50
	v_add_u32_e32 v43, s0, v0
	v_add_u32_e32 v82, s0, v42
	v_mad_u64_u32 v[6:7], s[0:1], v2, s2, v[4:5]
	v_mul_lo_u32 v41, v40, s2
	v_lshlrev_b32_e32 v45, 4, v45
	v_add3_u32 v83, v41, v45, 0
	v_lshrrev_b32_e32 v45, 5, v50
	s_movk_i32 s0, 0x2100
	v_and_b32_e32 v35, 28, v0
	v_or_b32_e32 v0, 62, v1
	v_or_b32_e32 v1, 63, v1
	v_mul_lo_u32 v84, v45, s0
	v_mul_lo_u32 v0, v0, s2
	v_mul_lo_u32 v44, v1, s2
	v_or_b32_e32 v10, 2, v2
	v_or_b32_e32 v12, 4, v2
	v_or_b32_e32 v14, 6, v2
	v_or_b32_e32 v16, 8, v2
	v_or_b32_e32 v18, 10, v2
	v_or_b32_e32 v20, 12, v2
	v_or_b32_e32 v22, 14, v2
	v_or_b32_e32 v24, 16, v2
	v_or_b32_e32 v26, 18, v2
	v_or_b32_e32 v28, 20, v2
	v_or_b32_e32 v30, 22, v2
	v_or_b32_e32 v32, 24, v2
	v_or_b32_e32 v34, 26, v2
	v_or_b32_e32 v36, 28, v2
	v_or_b32_e32 v38, 30, v2
	v_ashrrev_i32_e32 v41, 31, v40
	v_or_b32_e32 v42, v84, v42
	v_ashrrev_i32_e32 v3, 31, v2
	v_mov_b32_e32 v8, v2
	v_mov_b32_e32 v1, v2
	v_mov_b32_e32 v5, v10
	v_mov_b32_e32 v7, v12
	v_mov_b32_e32 v9, v14
	v_mov_b32_e32 v11, v16
	v_mov_b32_e32 v13, v18
	v_mov_b32_e32 v15, v20
	v_mov_b32_e32 v17, v22
	v_mov_b32_e32 v19, v24
	v_mov_b32_e32 v21, v26
	v_mov_b32_e32 v23, v28
	v_mov_b32_e32 v25, v30
	v_mov_b32_e32 v27, v32
	v_mov_b32_e32 v29, v34
	v_mov_b32_e32 v31, v36
	v_mov_b32_e32 v33, v38
	v_lshlrev_b64 v[40:41], 2, v[40:41]
	v_add_u32_e32 v42, 0, v42
	v_mov_b32_e32 v45, 0
	v_add_u32_e32 v85, v4, v0
	v_add_u32_e32 v86, v4, v44
	s_branch .Lwqd_112
.Lwqd_111:
	s_or_b64 exec, exec, s[0:1]
	s_waitcnt lgkmcnt(0)
	s_barrier
	ds_read_b32 v0, v82
	ds_read_b32 v44, v85
	ds_read_b32 v58, v86
	s_mov_b32 s2, 0x42fe0000
	v_add_u32_e32 v57, 0x400, v6
	s_waitcnt lgkmcnt(2)
	v_div_scale_f32 v46, s[0:1], v0, v0, s2
	v_rcp_f32_e32 v47, v46
	v_readlane_b32 s0, v116, 4
	v_readlane_b32 s1, v116, 5
	v_add_u32_e32 v60, 0x800, v6
	v_fma_f32 v48, -v46, v47, 1.0
	v_fmac_f32_e32 v47, v48, v47
	v_div_scale_f32 v48, vcc, s2, v0, s2
	v_mul_f32_e32 v49, v48, v47
	v_fma_f32 v52, -v46, v49, v48
	v_fmac_f32_e32 v49, v52, v47
	v_fma_f32 v46, -v46, v49, v48
	v_div_fmas_f32 v46, v46, v47, v49
	ds_read2_b32 v[48:49], v6 offset1:33
	v_div_fixup_f32 v46, v46, v0, s2
	v_cmp_lt_f32_e32 vcc, 0, v0
	ds_read2_b32 v[52:53], v6 offset0:66 offset1:99
	v_readlane_b32 s28, v116, 2
	v_cndmask_b32_e32 v0, 0, v46, vcc
	s_waitcnt lgkmcnt(1)
	v_mul_f32_e32 v48, v48, v0
	v_rndne_f32_e32 v48, v48
	v_cvt_i32_f32_e32 v54, v48
	v_mul_f32_e32 v48, v0, v49
	v_rndne_f32_e32 v48, v48
	v_cvt_i32_f32_e32 v55, v48
	s_waitcnt lgkmcnt(0)
	v_mul_f32_e32 v48, v0, v52
	v_rndne_f32_e32 v48, v48
	v_cvt_i32_f32_sdwa v52, v48 dst_sel:WORD_1 dst_unused:UNUSED_PAD src0_sel:DWORD
	v_mul_f32_e32 v48, v0, v53
	v_or_b32_e32 v46, s33, v37
	v_rndne_f32_e32 v48, v48
	v_ashrrev_i32_e32 v47, 31, v46
	v_cvt_i32_f32_sdwa v53, v48 dst_sel:BYTE_3 dst_unused:UNUSED_PAD src0_sel:DWORD
	ds_read2_b32 v[48:49], v6 offset0:132 offset1:165
	v_lshlrev_b64 v[46:47], 10, v[46:47]
	v_lshl_add_u64 v[46:47], s[0:1], 0, v[46:47]
	v_lshlrev_b32_e32 v55, 8, v55
	s_mov_b32 s0, 0xc0c0500
	v_perm_b32 v54, v55, v54, s0
	v_and_b32_e32 v52, 0xff0000, v52
	v_or3_b32 v52, v54, v52, v53
	ds_read2_b32 v[54:55], v6 offset0:198 offset1:231
	s_waitcnt lgkmcnt(1)
	v_mul_f32_e32 v48, v0, v48
	v_rndne_f32_e32 v48, v48
	v_cvt_i32_f32_e32 v53, v48
	v_mul_f32_e32 v48, v0, v49
	v_rndne_f32_e32 v48, v48
	v_cvt_i32_f32_e32 v56, v48
	s_waitcnt lgkmcnt(0)
	v_mul_f32_e32 v48, v0, v54
	v_rndne_f32_e32 v48, v48
	v_cvt_i32_f32_sdwa v54, v48 dst_sel:WORD_1 dst_unused:UNUSED_PAD src0_sel:DWORD
	v_mul_f32_e32 v48, v0, v55
	v_rndne_f32_e32 v48, v48
	v_cvt_i32_f32_sdwa v55, v48 dst_sel:BYTE_3 dst_unused:UNUSED_PAD src0_sel:DWORD
	ds_read2_b32 v[48:49], v57 offset0:8 offset1:41
	v_lshlrev_b32_e32 v56, 8, v56
	v_perm_b32 v53, v56, v53, s0
	v_and_b32_e32 v54, 0xff0000, v54
	v_or3_b32 v53, v53, v54, v55
	ds_read2_b32 v[54:55], v57 offset0:74 offset1:107
	s_waitcnt lgkmcnt(1)
	v_mul_f32_e32 v48, v0, v48
	v_rndne_f32_e32 v48, v48
	v_cvt_i32_f32_e32 v56, v48
	v_mul_f32_e32 v48, v0, v49
	v_rndne_f32_e32 v48, v48
	v_cvt_i32_f32_e32 v59, v48
	s_waitcnt lgkmcnt(0)
	v_mul_f32_e32 v48, v0, v54
	v_rndne_f32_e32 v48, v48
	v_cvt_i32_f32_sdwa v54, v48 dst_sel:WORD_1 dst_unused:UNUSED_PAD src0_sel:DWORD
	v_mul_f32_e32 v48, v0, v55
	v_rndne_f32_e32 v48, v48
	v_cvt_i32_f32_sdwa v55, v48 dst_sel:BYTE_3 dst_unused:UNUSED_PAD src0_sel:DWORD
	ds_read2_b32 v[48:49], v57 offset0:140 offset1:173
	v_lshlrev_b32_e32 v59, 8, v59
	v_perm_b32 v56, v59, v56, s0
	v_and_b32_e32 v54, 0xff0000, v54
	v_or3_b32 v54, v56, v54, v55
	ds_read2_b32 v[56:57], v57 offset0:206 offset1:239
	s_waitcnt lgkmcnt(1)
	v_mul_f32_e32 v48, v0, v48
	v_mul_f32_e32 v49, v0, v49
	v_rndne_f32_e32 v48, v48
	v_rndne_f32_e32 v49, v49
	v_cvt_i32_f32_e32 v55, v48
	s_waitcnt lgkmcnt(0)
	v_mul_f32_e32 v48, v0, v56
	v_cvt_i32_f32_e32 v49, v49
	v_rndne_f32_e32 v48, v48
	v_cvt_i32_f32_sdwa v56, v48 dst_sel:WORD_1 dst_unused:UNUSED_PAD src0_sel:DWORD
	v_mul_f32_e32 v48, v0, v57
	v_rndne_f32_e32 v48, v48
	v_cvt_i32_f32_sdwa v57, v48 dst_sel:BYTE_3 dst_unused:UNUSED_PAD src0_sel:DWORD
	v_lshlrev_b32_e32 v59, 8, v49
	ds_read2_b32 v[48:49], v60 offset0:16 offset1:49
	v_perm_b32 v55, v59, v55, s0
	v_and_b32_e32 v56, 0xff0000, v56
	v_lshl_add_u64 v[46:47], v[46:47], 0, v[2:3]
	v_or3_b32 v55, v55, v56, v57
	global_store_dwordx4 v[46:47], v[52:55], off
	ds_read2_b32 v[52:53], v60 offset0:82 offset1:115
	s_waitcnt lgkmcnt(1)
	v_mul_f32_e32 v48, v0, v48
	v_rndne_f32_e32 v48, v48
	v_cvt_i32_f32_e32 v54, v48
	v_mul_f32_e32 v48, v0, v49
	v_rndne_f32_e32 v48, v48
	v_cvt_i32_f32_e32 v55, v48
	s_waitcnt lgkmcnt(0)
	v_mul_f32_e32 v48, v0, v52
	v_rndne_f32_e32 v48, v48
	v_cvt_i32_f32_sdwa v52, v48 dst_sel:WORD_1 dst_unused:UNUSED_PAD src0_sel:DWORD
	v_mul_f32_e32 v48, v0, v53
	v_rndne_f32_e32 v48, v48
	v_cvt_i32_f32_sdwa v53, v48 dst_sel:BYTE_3 dst_unused:UNUSED_PAD src0_sel:DWORD
	ds_read2_b32 v[48:49], v60 offset0:148 offset1:181
	v_lshlrev_b32_e32 v55, 8, v55
	v_perm_b32 v54, v55, v54, s0
	v_and_b32_e32 v52, 0xff0000, v52
	v_or3_b32 v52, v54, v52, v53
	ds_read2_b32 v[54:55], v60 offset0:214 offset1:247
	s_waitcnt lgkmcnt(1)
	v_mul_f32_e32 v48, v0, v48
	v_rndne_f32_e32 v48, v48
	v_cvt_i32_f32_e32 v53, v48
	v_mul_f32_e32 v48, v0, v49
	v_rndne_f32_e32 v48, v48
	v_cvt_i32_f32_e32 v56, v48
	s_waitcnt lgkmcnt(0)
	v_mul_f32_e32 v48, v0, v54
	v_rndne_f32_e32 v48, v48
	v_cvt_i32_f32_sdwa v54, v48 dst_sel:WORD_1 dst_unused:UNUSED_PAD src0_sel:DWORD
	v_mul_f32_e32 v48, v0, v55
	v_rndne_f32_e32 v48, v48
	v_add_u32_e32 v57, 0xc00, v6
	v_cvt_i32_f32_sdwa v55, v48 dst_sel:BYTE_3 dst_unused:UNUSED_PAD src0_sel:DWORD
	ds_read2_b32 v[48:49], v57 offset0:24 offset1:57
	v_lshlrev_b32_e32 v56, 8, v56
	v_perm_b32 v53, v56, v53, s0
	v_and_b32_e32 v54, 0xff0000, v54
	v_or3_b32 v53, v53, v54, v55
	ds_read2_b32 v[54:55], v57 offset0:90 offset1:123
	s_waitcnt lgkmcnt(1)
	v_mul_f32_e32 v48, v0, v48
	v_rndne_f32_e32 v48, v48
	v_cvt_i32_f32_e32 v56, v48
	v_mul_f32_e32 v48, v0, v49
	v_rndne_f32_e32 v48, v48
	v_cvt_i32_f32_e32 v59, v48
	s_waitcnt lgkmcnt(0)
	v_mul_f32_e32 v48, v0, v54
	v_rndne_f32_e32 v48, v48
	v_cvt_i32_f32_sdwa v54, v48 dst_sel:WORD_1 dst_unused:UNUSED_PAD src0_sel:DWORD
	v_mul_f32_e32 v48, v0, v55
	v_rndne_f32_e32 v48, v48
	v_cvt_i32_f32_sdwa v55, v48 dst_sel:BYTE_3 dst_unused:UNUSED_PAD src0_sel:DWORD
	ds_read2_b32 v[48:49], v57 offset0:156 offset1:189
	v_lshlrev_b32_e32 v59, 8, v59
	v_perm_b32 v56, v59, v56, s0
	v_and_b32_e32 v54, 0xff0000, v54
	v_or3_b32 v54, v56, v54, v55
	ds_read2_b32 v[56:57], v57 offset0:222 offset1:255
	s_waitcnt lgkmcnt(1)
	v_mul_f32_e32 v48, v0, v48
	v_mul_f32_e32 v49, v0, v49
	v_rndne_f32_e32 v48, v48
	v_rndne_f32_e32 v49, v49
	v_cvt_i32_f32_e32 v55, v48
	s_waitcnt lgkmcnt(0)
	v_mul_f32_e32 v48, v0, v56
	v_cvt_i32_f32_e32 v49, v49
	v_rndne_f32_e32 v48, v48
	v_cvt_i32_f32_sdwa v56, v48 dst_sel:WORD_1 dst_unused:UNUSED_PAD src0_sel:DWORD
	v_mul_f32_e32 v48, v0, v57
	v_rndne_f32_e32 v48, v48
	v_cvt_i32_f32_sdwa v57, v48 dst_sel:BYTE_3 dst_unused:UNUSED_PAD src0_sel:DWORD
	v_add_u32_e32 v60, 0x1000, v6
	v_lshlrev_b32_e32 v59, 8, v49
	ds_read2_b32 v[48:49], v60 offset0:32 offset1:65
	v_perm_b32 v55, v59, v55, s0
	v_and_b32_e32 v56, 0xff0000, v56
	v_or3_b32 v55, v55, v56, v57
	global_store_dwordx4 v[46:47], v[52:55], off offset:16
	ds_read2_b32 v[52:53], v60 offset0:98 offset1:131
	s_waitcnt lgkmcnt(1)
	v_mul_f32_e32 v48, v0, v48
	v_rndne_f32_e32 v48, v48
	v_cvt_i32_f32_e32 v54, v48
	v_mul_f32_e32 v48, v0, v49
	v_rndne_f32_e32 v48, v48
	v_cvt_i32_f32_e32 v55, v48
	s_waitcnt lgkmcnt(0)
	v_mul_f32_e32 v48, v0, v52
	v_rndne_f32_e32 v48, v48
	v_cvt_i32_f32_sdwa v52, v48 dst_sel:WORD_1 dst_unused:UNUSED_PAD src0_sel:DWORD
	v_mul_f32_e32 v48, v0, v53
	v_rndne_f32_e32 v48, v48
	v_cvt_i32_f32_sdwa v53, v48 dst_sel:BYTE_3 dst_unused:UNUSED_PAD src0_sel:DWORD
	ds_read2_b32 v[48:49], v60 offset0:164 offset1:197
	v_lshlrev_b32_e32 v55, 8, v55
	v_perm_b32 v54, v55, v54, s0
	v_and_b32_e32 v52, 0xff0000, v52
	v_or3_b32 v52, v54, v52, v53
	v_add_u32_e32 v53, 0x1200, v6
	ds_read2_b32 v[54:55], v53 offset0:102 offset1:135
	s_waitcnt lgkmcnt(1)
	v_mul_f32_e32 v48, v0, v48
	v_rndne_f32_e32 v48, v48
	v_cvt_i32_f32_e32 v53, v48
	v_mul_f32_e32 v48, v0, v49
	v_rndne_f32_e32 v48, v48
	v_cvt_i32_f32_e32 v56, v48
	s_waitcnt lgkmcnt(0)
	v_mul_f32_e32 v48, v0, v54
	v_rndne_f32_e32 v48, v48
	v_cvt_i32_f32_sdwa v54, v48 dst_sel:WORD_1 dst_unused:UNUSED_PAD src0_sel:DWORD
	v_mul_f32_e32 v48, v0, v55
	v_rndne_f32_e32 v48, v48
	v_add_u32_e32 v57, 0x1400, v6
	v_cvt_i32_f32_sdwa v55, v48 dst_sel:BYTE_3 dst_unused:UNUSED_PAD src0_sel:DWORD
	ds_read2_b32 v[48:49], v57 offset0:40 offset1:73
	v_lshlrev_b32_e32 v56, 8, v56
	v_perm_b32 v53, v56, v53, s0
	v_and_b32_e32 v54, 0xff0000, v54
	v_or3_b32 v53, v53, v54, v55
	ds_read2_b32 v[54:55], v57 offset0:106 offset1:139
	s_waitcnt lgkmcnt(1)
	v_mul_f32_e32 v48, v0, v48
	v_rndne_f32_e32 v48, v48
	v_cvt_i32_f32_e32 v56, v48
	v_mul_f32_e32 v48, v0, v49
	v_rndne_f32_e32 v48, v48
	v_cvt_i32_f32_e32 v59, v48
	s_waitcnt lgkmcnt(0)
	v_mul_f32_e32 v48, v0, v54
	v_rndne_f32_e32 v48, v48
	v_cvt_i32_f32_sdwa v54, v48 dst_sel:WORD_1 dst_unused:UNUSED_PAD src0_sel:DWORD
	v_mul_f32_e32 v48, v0, v55
	v_rndne_f32_e32 v48, v48
	v_cvt_i32_f32_sdwa v55, v48 dst_sel:BYTE_3 dst_unused:UNUSED_PAD src0_sel:DWORD
	ds_read2_b32 v[48:49], v57 offset0:172 offset1:205
	v_lshlrev_b32_e32 v57, 8, v59
	v_perm_b32 v56, v57, v56, s0
	v_and_b32_e32 v54, 0xff0000, v54
	v_or3_b32 v54, v56, v54, v55
	v_add_u32_e32 v55, 0x1600, v6
	ds_read2_b32 v[56:57], v55 offset0:110 offset1:143
	s_waitcnt lgkmcnt(1)
	v_mul_f32_e32 v48, v0, v48
	v_mul_f32_e32 v49, v0, v49
	v_rndne_f32_e32 v48, v48
	v_rndne_f32_e32 v49, v49
	v_cvt_i32_f32_e32 v55, v48
	s_waitcnt lgkmcnt(0)
	v_mul_f32_e32 v48, v0, v56
	v_cvt_i32_f32_e32 v49, v49
	v_rndne_f32_e32 v48, v48
	v_cvt_i32_f32_sdwa v56, v48 dst_sel:WORD_1 dst_unused:UNUSED_PAD src0_sel:DWORD
	v_mul_f32_e32 v48, v0, v57
	v_rndne_f32_e32 v48, v48
	v_cvt_i32_f32_sdwa v57, v48 dst_sel:BYTE_3 dst_unused:UNUSED_PAD src0_sel:DWORD
	v_add_u32_e32 v60, 0x1800, v6
	v_lshlrev_b32_e32 v59, 8, v49
	ds_read2_b32 v[48:49], v60 offset0:48 offset1:81
	v_perm_b32 v55, v59, v55, s0
	v_and_b32_e32 v56, 0xff0000, v56
	v_or3_b32 v55, v55, v56, v57
	global_store_dwordx4 v[46:47], v[52:55], off offset:32
	ds_read2_b32 v[52:53], v60 offset0:114 offset1:147
	s_waitcnt lgkmcnt(1)
	v_mul_f32_e32 v48, v0, v48
	v_rndne_f32_e32 v48, v48
	v_cvt_i32_f32_e32 v54, v48
	v_mul_f32_e32 v48, v0, v49
	v_rndne_f32_e32 v48, v48
	v_cvt_i32_f32_e32 v55, v48
	s_waitcnt lgkmcnt(0)
	v_mul_f32_e32 v48, v0, v52
	v_rndne_f32_e32 v48, v48
	v_cvt_i32_f32_sdwa v52, v48 dst_sel:WORD_1 dst_unused:UNUSED_PAD src0_sel:DWORD
	v_mul_f32_e32 v48, v0, v53
	v_rndne_f32_e32 v48, v48
	v_cvt_i32_f32_sdwa v53, v48 dst_sel:BYTE_3 dst_unused:UNUSED_PAD src0_sel:DWORD
	ds_read2_b32 v[48:49], v60 offset0:180 offset1:213
	v_lshlrev_b32_e32 v55, 8, v55
	v_perm_b32 v54, v55, v54, s0
	v_and_b32_e32 v52, 0xff0000, v52
	v_or3_b32 v52, v54, v52, v53
	v_add_u32_e32 v53, 0x1a00, v6
	ds_read2_b32 v[54:55], v53 offset0:118 offset1:151
	s_waitcnt lgkmcnt(1)
	v_mul_f32_e32 v48, v0, v48
	v_rndne_f32_e32 v48, v48
	v_cvt_i32_f32_e32 v53, v48
	v_mul_f32_e32 v48, v0, v49
	v_rndne_f32_e32 v48, v48
	v_cvt_i32_f32_e32 v56, v48
	s_waitcnt lgkmcnt(0)
	v_mul_f32_e32 v48, v0, v54
	v_rndne_f32_e32 v48, v48
	v_cvt_i32_f32_sdwa v54, v48 dst_sel:WORD_1 dst_unused:UNUSED_PAD src0_sel:DWORD
	v_mul_f32_e32 v48, v0, v55
	v_rndne_f32_e32 v48, v48
	v_add_u32_e32 v57, 0x1c00, v6
	v_cvt_i32_f32_sdwa v55, v48 dst_sel:BYTE_3 dst_unused:UNUSED_PAD src0_sel:DWORD
	ds_read2_b32 v[48:49], v57 offset0:56 offset1:89
	v_lshlrev_b32_e32 v56, 8, v56
	v_perm_b32 v53, v56, v53, s0
	v_and_b32_e32 v54, 0xff0000, v54
	v_or3_b32 v53, v53, v54, v55
	ds_read2_b32 v[54:55], v57 offset0:122 offset1:155
	s_waitcnt lgkmcnt(1)
	v_mul_f32_e32 v48, v0, v48
	v_rndne_f32_e32 v48, v48
	v_cvt_i32_f32_e32 v56, v48
	v_mul_f32_e32 v48, v0, v49
	v_rndne_f32_e32 v48, v48
	v_cvt_i32_f32_e32 v59, v48
	s_waitcnt lgkmcnt(0)
	v_mul_f32_e32 v48, v0, v54
	v_rndne_f32_e32 v48, v48
	v_cvt_i32_f32_sdwa v54, v48 dst_sel:WORD_1 dst_unused:UNUSED_PAD src0_sel:DWORD
	v_mul_f32_e32 v48, v0, v55
	v_rndne_f32_e32 v48, v48
	v_cvt_i32_f32_sdwa v55, v48 dst_sel:BYTE_3 dst_unused:UNUSED_PAD src0_sel:DWORD
	ds_read2_b32 v[48:49], v57 offset0:188 offset1:221
	v_mul_f32_e32 v44, v0, v44
	v_rndne_f32_e32 v44, v44
	v_cvt_i32_f32_sdwa v44, v44 dst_sel:WORD_1 dst_unused:UNUSED_PAD src0_sel:DWORD
	v_lshlrev_b32_e32 v57, 8, v59
	s_waitcnt lgkmcnt(0)
	v_mul_f32_e32 v49, v0, v49
	v_mul_f32_e32 v48, v0, v48
	v_rndne_f32_e32 v49, v49
	v_rndne_f32_e32 v48, v48
	v_cvt_i32_f32_e32 v49, v49
	v_cvt_i32_f32_e32 v48, v48
	v_mul_f32_e32 v0, v0, v58
	v_rndne_f32_e32 v0, v0
	v_cvt_i32_f32_sdwa v0, v0 dst_sel:BYTE_3 dst_unused:UNUSED_PAD src0_sel:DWORD
	v_lshlrev_b32_e32 v49, 8, v49
	v_perm_b32 v56, v57, v56, s0
	v_perm_b32 v48, v49, v48, s0
	s_add_i32 s98, s98, s100
	v_and_b32_e32 v54, 0xff0000, v54
	v_and_b32_e32 v44, 0xff0000, v44
	s_mov_b32 s0, 0xfffff530
	s_cmp_lt_u32 s98, 0x1330
	s_cselect_b32 s0, 0x30, s0
	s_cmp_lt_u32 s98, 0x1310
	s_cselect_b32 s0, 0xffffffd0, s0
	s_cmp_lt_u32 s98, 0x1230
	s_cselect_b32 s0, 0xffffef30, s0
	s_cmp_lt_u32 s98, 0x1180
	s_cselect_b32 s0, 0xfffff2a0, s0
	s_cmp_lt_u32 s98, 0xfa0
	s_cselect_b32 s0, 0xfffff2a0, s0
	s_cmp_lt_u32 s98, 0xec0
	s_cselect_b32 s0, 0x460, s0
	s_cmp_lt_u32 s98, 0xea0
	s_cselect_b32 s0, 0x280, s0
	s_cmp_lt_u32 s98, 0xdc0
	s_cselect_b32 s0, 0x1a0, s0
	s_cmp_lt_u32 s98, 0x6f0
	s_cselect_b32 s0, 0xc50, s0
	s_cmp_lt_u32 s98, 0x6d0
	s_cselect_b32 s0, 0xb30, s0
	s_cmp_lt_u32 s98, 0x5f0
	s_cselect_b32 s0, 0x270, s0
	s_cmp_lt_u32 s98, 0x1b0
	s_cselect_b32 s0, 0x1150, s0
	s_cmp_lt_u32 s98, 0x190
	s_cselect_b32 s0, 0xeb0, s0
	s_cmp_lt_u32 s98, 0xb0
	s_cselect_b32 s0, 0x0, s0
	s_add_i32 s28, s98, s0
	v_or3_b32 v54, v56, v54, v55
	v_or3_b32 v55, v48, v44, v0
	s_cmp_ge_u32 s98, s99
	global_store_dwordx4 v[46:47], v[52:55], off offset:48
	s_barrier
	s_cbranch_scc1 .Lwqd_exit

.Lwqd_124:
	s_ashr_i32 s3, s2, 31
	v_writelane_b32 v116, s28, 2
	s_cmp_lt_i32 s9, 2
	s_mov_b64 s[4:5], -1
	s_cbranch_scc1 .Lwqd_129
	s_cmp_gt_i32 s9, 2
	s_cbranch_scc0 .Lwqd_127
	v_readlane_b32 s12, v251, 44
	v_readlane_b32 s18, v251, 50
	v_readlane_b32 s19, v251, 51
	s_lshl_b64 s[4:5], s[2:3], 20
	s_lshl_b64 s[0:1], s[2:3], 22
	s_mov_b64 s[10:11], s[18:19]
	s_add_u32 s0, s10, s0
	s_addc_u32 s1, s11, s1
	v_readlane_b32 s6, v252, 12
	s_add_u32 s6, s6, s4
	v_readlane_b32 s4, v252, 13
	s_addc_u32 s7, s4, s5
	v_writelane_b32 v116, s6, 4
	s_lshl_b64 s[4:5], s[2:3], 12
	v_readlane_b32 s13, v251, 45
	v_writelane_b32 v116, s7, 5
	v_readlane_b32 s14, v251, 46
	v_readlane_b32 s3, v252, 14
	s_add_u32 s4, s3, s4
	v_readlane_b32 s3, v252, 15
	s_addc_u32 s5, s3, s5
	v_writelane_b32 v116, s4, 6
	v_readlane_b32 s15, v251, 47
	v_readlane_b32 s16, v251, 48
	v_readlane_b32 s17, v251, 49
	v_readlane_b32 s20, v251, 52
	v_readlane_b32 s21, v251, 53
	v_readlane_b32 s22, v251, 54
	v_readlane_b32 s23, v251, 55
	v_readlane_b32 s24, v251, 56
	v_readlane_b32 s25, v251, 57
	v_readlane_b32 s26, v251, 58
	v_readlane_b32 s27, v251, 59
	v_writelane_b32 v116, s5, 7
	s_mov_b64 s[4:5], 0
.Lwqd_127:
	s_andn2_b64 vcc, exec, s[4:5]
	s_cbranch_vccnz .Lwqd_134
	s_mul_i32 s0, s2, 0x1b10000
	s_mul_hi_i32 s1, s2, 0x1b10000
	s_add_u32 s0, s52, s0
	s_addc_u32 s1, s53, s1
	s_mul_i32 s4, s2, 0x700000
	v_readlane_b32 s5, v251, 62
	s_mul_hi_i32 s3, s2, 0x700000
	s_add_u32 s6, s5, s4
	v_readlane_b32 s4, v251, 63
	s_addc_u32 s7, s4, s3
	v_writelane_b32 v116, s6, 4
	s_mul_i32 s4, s2, 0x7000
	s_mul_hi_i32 s3, s2, 0x7000
	v_writelane_b32 v116, s7, 5
	s_mov_b32 s10, 1
	v_readlane_b32 s5, v252, 16
	s_add_u32 s6, s5, s4
	v_readlane_b32 s4, v252, 17
	s_addc_u32 s7, s4, s3
	v_writelane_b32 v116, s6, 6
	s_nop 1
	v_writelane_b32 v116, s7, 7
	s_mov_b64 s[6:7], 0x1b10
	s_mov_b32 s4, 0
	s_cbranch_execnz .Lwqd_135
	s_branch .Lwqd_130

.Lwqd_130:
	s_cmp_eq_u32 s9, 1
	s_mov_b64 s[4:5], -1
	s_cbranch_scc1 .Lwqd_132
	v_readlane_b32 s12, v251, 44
	v_readlane_b32 s13, v251, 45
	v_readlane_b32 s14, v251, 46
	v_readlane_b32 s15, v251, 47
	v_readlane_b32 s16, v251, 48
	v_readlane_b32 s17, v251, 49
	v_readlane_b32 s18, v251, 50
	v_readlane_b32 s19, v251, 51
	v_readlane_b32 s20, v251, 52
	v_readlane_b32 s21, v251, 53
	s_mul_i32 s0, s2, 0x1600000
	v_readlane_b32 s22, v251, 54
	v_readlane_b32 s23, v251, 55
	v_readlane_b32 s24, v251, 56
	v_readlane_b32 s25, v251, 57
	v_readlane_b32 s26, v251, 58
	v_readlane_b32 s27, v251, 59
	s_mov_b64 s[12:13], s[20:21]
	s_mul_hi_i32 s1, s2, 0x1600000
	s_add_u32 s0, s12, s0
	s_addc_u32 s1, s13, s1
	s_mul_i32 s4, s2, 0x580000
	v_readlane_b32 s5, v252, 22
	s_mul_hi_i32 s3, s2, 0x580000
	s_add_u32 s6, s5, s4
	v_readlane_b32 s4, v252, 23
	s_addc_u32 s7, s4, s3
	v_writelane_b32 v116, s6, 4
	s_mul_i32 s4, s2, 0x5800
	s_mul_hi_i32 s3, s2, 0x5800
	v_writelane_b32 v116, s7, 5
	s_mov_b64 s[14:15], s[22:23]
	v_readlane_b32 s5, v252, 24
	s_add_u32 s6, s5, s4
	v_readlane_b32 s4, v252, 25
	s_addc_u32 s7, s4, s3
	v_writelane_b32 v116, s6, 6
	s_mov_b64 s[4:5], 0
	s_mov_b64 s[16:17], s[24:25]
	v_writelane_b32 v116, s7, 7
	s_mov_b64 s[18:19], s[26:27]
.Lwqd_132:
	s_andn2_b64 vcc, exec, s[4:5]
	s_cbranch_vccnz .Lwqd_136
	v_readlane_b32 s12, v251, 44
	v_readlane_b32 s13, v251, 45
	v_readlane_b32 s14, v251, 46
	v_readlane_b32 s15, v251, 47
	v_readlane_b32 s16, v251, 48
	v_readlane_b32 s17, v251, 49
	v_readlane_b32 s18, v251, 50
	v_readlane_b32 s19, v251, 51
	v_readlane_b32 s20, v251, 52
	v_readlane_b32 s21, v251, 53
	v_readlane_b32 s22, v251, 54
	v_readlane_b32 s23, v251, 55
	v_readlane_b32 s24, v251, 56
	v_readlane_b32 s25, v251, 57
	v_readlane_b32 s26, v251, 58
	v_readlane_b32 s27, v251, 59
	s_mov_b64 s[12:13], s[20:21]
	s_mul_i32 s0, s2, 0x1c00000
	s_mov_b64 s[18:19], s[26:27]
	s_mul_hi_i32 s1, s2, 0x1c00000
	s_add_u32 s0, s18, s0
	s_addc_u32 s1, s19, s1
	s_mul_i32 s4, s2, 0x700000
	v_readlane_b32 s5, v252, 18
	s_mul_hi_i32 s3, s2, 0x700000
	s_add_u32 s6, s5, s4
	v_readlane_b32 s4, v252, 19
	s_addc_u32 s7, s4, s3
	v_writelane_b32 v116, s6, 4
	s_mul_hi_i32 s3, s2, 0x7000
	s_mulk_i32 s2, 0x7000
	v_writelane_b32 v116, s7, 5
	s_mov_b64 s[6:7], 0x1c00
	v_readlane_b32 s4, v252, 20
	s_add_u32 s4, s4, s2
	v_readlane_b32 s2, v252, 21
	s_addc_u32 s5, s2, s3
	v_writelane_b32 v116, s4, 6
	s_mov_b64 s[14:15], s[22:23]
	s_mov_b64 s[16:17], s[24:25]
	v_writelane_b32 v116, s5, 7
	s_movk_i32 s4, 0xe00
	s_branch .Lwqd_137

.Lwqd_149:
	v_max_i32_e32 v44, 0, v46
	v_cmp_gt_i32_e32 vcc, 0, v46
	v_lshlrev_b64 v[46:47], 2, v[44:45]
	v_mul_lo_u32 v0, v40, s7
	v_mul_lo_u32 v44, v41, s6
	v_mad_u64_u32 v[46:47], s[2:3], v40, s6, v[46:47]
	v_add3_u32 v47, v44, v47, v0
	v_writelane_b32 v116, s9, 8
	s_mov_b32 s4, 0
	v_lshl_add_u64 v[46:47], s[0:1], 0, v[46:47]
	s_lshl_b64 s[0:1], s[6:7], 11
	s_lshl_b64 s[2:3], s[6:7], 8
.Lwqd_150:
	global_load_dwordx4 v[52:55], v[46:47], off
	v_lshl_add_u64 v[48:49], v[46:47], 0, s[2:3]
	global_load_dwordx4 v[56:59], v[48:49], off
	v_lshl_add_u64 v[48:49], v[48:49], 0, s[2:3]
	global_load_dwordx4 v[60:63], v[48:49], off
	v_lshl_add_u64 v[48:49], v[48:49], 0, s[2:3]
	global_load_dwordx4 v[64:67], v[48:49], off
	v_lshl_add_u64 v[48:49], v[48:49], 0, s[2:3]
	global_load_dwordx4 v[68:71], v[48:49], off
	v_lshl_add_u64 v[48:49], v[48:49], 0, s[2:3]
	global_load_dwordx4 v[72:75], v[48:49], off
	v_lshl_add_u64 v[48:49], v[48:49], 0, s[2:3]
	global_load_dwordx4 v[76:79], v[48:49], off
	v_lshl_add_u64 v[48:49], v[48:49], 0, s[2:3]
	global_load_dwordx4 v[88:91], v[48:49], off
	v_lshl_add_u64 v[46:47], v[46:47], 0, s[0:1]
	global_load_dwordx4 v[132:135], v[46:47], off
	v_lshl_add_u64 v[164:165], v[46:47], 0, s[2:3]
	global_load_dwordx4 v[136:139], v[164:165], off
	v_lshl_add_u64 v[164:165], v[164:165], 0, s[2:3]
	global_load_dwordx4 v[140:143], v[164:165], off
	v_lshl_add_u64 v[164:165], v[164:165], 0, s[2:3]
	global_load_dwordx4 v[144:147], v[164:165], off
	v_lshl_add_u64 v[164:165], v[164:165], 0, s[2:3]
	global_load_dwordx4 v[148:151], v[164:165], off
	v_lshl_add_u64 v[164:165], v[164:165], 0, s[2:3]
	global_load_dwordx4 v[152:155], v[164:165], off
	v_lshl_add_u64 v[164:165], v[164:165], 0, s[2:3]
	global_load_dwordx4 v[156:159], v[164:165], off
	v_lshl_add_u64 v[164:165], v[164:165], 0, s[2:3]
	global_load_dwordx4 v[160:163], v[164:165], off
	v_lshl_add_u64 v[46:47], v[46:47], 0, s[0:1]
	v_add_u32_e32 v0, s4, v83
	v_add_u32_e32 v44, 0x2100, v0
	v_add_u32_e32 v48, 0x2108, v0
	v_add_u32_e32 v49, 0x4200, v0
	v_add_u32_e32 v80, 0x4208, v0
	v_add_u32_e32 v81, 0x6300, v0
	v_add_u32_e32 v87, 0x6308, v0
	v_add_u32_e32 v92, 0x8400, v0
	v_add_u32_e32 v93, 0x8408, v0
	v_add_u32_e32 v94, 0xa500, v0
	v_add_u32_e32 v95, 0xa508, v0
	v_add_u32_e32 v96, 0xc600, v0
	v_add_u32_e32 v97, 0xc608, v0
	v_add_u32_e32 v98, 0xe700, v0
	v_add_u32_e32 v99, 0xe708, v0
	s_waitcnt vmcnt(15)
	v_cndmask_b32_e64 v54, v54, 0, vcc
	v_cndmask_b32_e64 v53, v53, 0, vcc
	v_cndmask_b32_e64 v52, v52, 0, vcc
	v_cndmask_b32_e64 v55, v55, 0, vcc
	ds_write2_b32 v0, v52, v53 offset1:1
	ds_write2_b32 v0, v54, v55 offset0:2 offset1:3
	s_waitcnt vmcnt(14)
	v_cndmask_b32_e64 v52, v58, 0, vcc
	v_cndmask_b32_e64 v53, v57, 0, vcc
	v_cndmask_b32_e64 v54, v56, 0, vcc
	v_cndmask_b32_e64 v0, v59, 0, vcc
	ds_write2_b32 v44, v54, v53 offset1:1
	ds_write2_b32 v48, v52, v0 offset1:1
	s_waitcnt vmcnt(13)
	v_cndmask_b32_e64 v48, v61, 0, vcc
	v_cndmask_b32_e64 v52, v60, 0, vcc
	v_cndmask_b32_e64 v0, v63, 0, vcc
	v_cndmask_b32_e64 v44, v62, 0, vcc
	ds_write2_b32 v49, v52, v48 offset1:1
	ds_write2_b32 v80, v44, v0 offset1:1
	s_waitcnt vmcnt(12)
	v_cndmask_b32_e64 v48, v65, 0, vcc
	v_cndmask_b32_e64 v49, v64, 0, vcc
	v_cndmask_b32_e64 v0, v67, 0, vcc
	v_cndmask_b32_e64 v44, v66, 0, vcc
	ds_write2_b32 v81, v49, v48 offset1:1
	ds_write2_b32 v87, v44, v0 offset1:1
	s_waitcnt vmcnt(11)
	v_cndmask_b32_e64 v48, v69, 0, vcc
	v_cndmask_b32_e64 v49, v68, 0, vcc
	v_cndmask_b32_e64 v0, v71, 0, vcc
	v_cndmask_b32_e64 v44, v70, 0, vcc
	ds_write2_b32 v92, v49, v48 offset1:1
	ds_write2_b32 v93, v44, v0 offset1:1
	s_waitcnt vmcnt(10)
	v_cndmask_b32_e64 v48, v73, 0, vcc
	v_cndmask_b32_e64 v49, v72, 0, vcc
	v_cndmask_b32_e64 v0, v75, 0, vcc
	v_cndmask_b32_e64 v44, v74, 0, vcc
	ds_write2_b32 v94, v49, v48 offset1:1
	ds_write2_b32 v95, v44, v0 offset1:1
	s_waitcnt vmcnt(9)
	v_cndmask_b32_e64 v48, v77, 0, vcc
	v_cndmask_b32_e64 v49, v76, 0, vcc
	v_cndmask_b32_e64 v0, v79, 0, vcc
	v_cndmask_b32_e64 v44, v78, 0, vcc
	ds_write2_b32 v96, v49, v48 offset1:1
	ds_write2_b32 v97, v44, v0 offset1:1
	s_waitcnt vmcnt(8)
	v_cndmask_b32_e64 v48, v89, 0, vcc
	v_cndmask_b32_e64 v49, v88, 0, vcc
	v_cndmask_b32_e64 v0, v91, 0, vcc
	v_cndmask_b32_e64 v44, v90, 0, vcc
	ds_write2_b32 v98, v49, v48 offset1:1
	ds_write2_b32 v99, v44, v0 offset1:1
	s_add_i32 s4, s4, 0x10800
	v_add_u32_e32 v0, s4, v83
	v_add_u32_e32 v44, 0x2100, v0
	v_add_u32_e32 v48, 0x2108, v0
	v_add_u32_e32 v49, 0x4200, v0
	v_add_u32_e32 v80, 0x4208, v0
	v_add_u32_e32 v81, 0x6300, v0
	v_add_u32_e32 v87, 0x6308, v0
	v_add_u32_e32 v92, 0x8400, v0
	v_add_u32_e32 v93, 0x8408, v0
	v_add_u32_e32 v94, 0xa500, v0
	v_add_u32_e32 v95, 0xa508, v0
	v_add_u32_e32 v96, 0xc600, v0
	v_add_u32_e32 v97, 0xc608, v0
	v_add_u32_e32 v98, 0xe700, v0
	v_add_u32_e32 v99, 0xe708, v0
	s_waitcnt vmcnt(7)
	v_cndmask_b32_e64 v54, v134, 0, vcc
	v_cndmask_b32_e64 v53, v133, 0, vcc
	v_cndmask_b32_e64 v52, v132, 0, vcc
	v_cndmask_b32_e64 v55, v135, 0, vcc
	ds_write2_b32 v0, v52, v53 offset1:1
	ds_write2_b32 v0, v54, v55 offset0:2 offset1:3
	s_waitcnt vmcnt(6)
	v_cndmask_b32_e64 v52, v138, 0, vcc
	v_cndmask_b32_e64 v53, v137, 0, vcc
	v_cndmask_b32_e64 v54, v136, 0, vcc
	v_cndmask_b32_e64 v0, v139, 0, vcc
	ds_write2_b32 v44, v54, v53 offset1:1
	ds_write2_b32 v48, v52, v0 offset1:1
	s_waitcnt vmcnt(5)
	v_cndmask_b32_e64 v48, v141, 0, vcc
	v_cndmask_b32_e64 v52, v140, 0, vcc
	v_cndmask_b32_e64 v0, v143, 0, vcc
	v_cndmask_b32_e64 v44, v142, 0, vcc
	ds_write2_b32 v49, v52, v48 offset1:1
	ds_write2_b32 v80, v44, v0 offset1:1
	s_waitcnt vmcnt(4)
	v_cndmask_b32_e64 v48, v145, 0, vcc
	v_cndmask_b32_e64 v49, v144, 0, vcc
	v_cndmask_b32_e64 v0, v147, 0, vcc
	v_cndmask_b32_e64 v44, v146, 0, vcc
	ds_write2_b32 v81, v49, v48 offset1:1
	ds_write2_b32 v87, v44, v0 offset1:1
	s_waitcnt vmcnt(3)
	v_cndmask_b32_e64 v48, v149, 0, vcc
	v_cndmask_b32_e64 v49, v148, 0, vcc
	v_cndmask_b32_e64 v0, v151, 0, vcc
	v_cndmask_b32_e64 v44, v150, 0, vcc
	ds_write2_b32 v92, v49, v48 offset1:1
	ds_write2_b32 v93, v44, v0 offset1:1
	s_waitcnt vmcnt(2)
	v_cndmask_b32_e64 v48, v153, 0, vcc
	v_cndmask_b32_e64 v49, v152, 0, vcc
	v_cndmask_b32_e64 v0, v155, 0, vcc
	v_cndmask_b32_e64 v44, v154, 0, vcc
	ds_write2_b32 v94, v49, v48 offset1:1
	ds_write2_b32 v95, v44, v0 offset1:1
	s_waitcnt vmcnt(1)
	v_cndmask_b32_e64 v48, v157, 0, vcc
	v_cndmask_b32_e64 v49, v156, 0, vcc
	v_cndmask_b32_e64 v0, v159, 0, vcc
	v_cndmask_b32_e64 v44, v158, 0, vcc
	ds_write2_b32 v96, v49, v48 offset1:1
	ds_write2_b32 v97, v44, v0 offset1:1
	s_waitcnt vmcnt(0)
	v_cndmask_b32_e64 v48, v161, 0, vcc
	v_cndmask_b32_e64 v49, v160, 0, vcc
	v_cndmask_b32_e64 v0, v163, 0, vcc
	v_cndmask_b32_e64 v44, v162, 0, vcc
	ds_write2_b32 v98, v49, v48 offset1:1
	ds_write2_b32 v99, v44, v0 offset1:1
	s_add_i32 s4, s4, 0x10800
	s_cmp_eq_u32 s4, 0x21000
	s_mov_b32 s0, 1
	v_mov_b32_e32 v44, v45
	v_writelane_b32 v116, s0, 10
	s_mov_b32 s0, 0
	v_writelane_b32 v116, s0, 12
	s_movk_i32 s33, 0xffe0
	s_mov_b64 s[12:13], 0
	v_mov_b64_e32 v[70:71], v[44:45]
	s_waitcnt lgkmcnt(0)
	s_barrier
	s_branch .Lwqd_167

.Lwqd_154:
	v_readlane_b32 s82, v116, 24
	v_readlane_b32 s83, v116, 25
	s_or_b64 exec, exec, s[82:83]
	s_and_b64 s[82:83], s[50:51], exec
	s_and_b64 s[50:51], s[10:11], exec
	s_and_b64 s[10:11], s[84:85], exec
	s_xor_b64 s[84:85], exec, -1
	s_orn2_b64 s[4:5], s[4:5], exec

.Lwqd_165:
	v_readlane_b32 vcc_lo, v116, 18
	v_readlane_b32 vcc_hi, v116, 19
	s_or_b64 exec, exec, vcc
	s_andn2_b64 s[78:79], s[78:79], exec
	s_and_b64 s[10:11], s[10:11], exec
	s_or_b64 s[78:79], s[78:79], s[10:11]
	s_andn2_b64 s[10:11], s[76:77], exec
	s_and_b64 s[50:51], s[50:51], exec
	s_or_b64 s[76:77], s[10:11], s[50:51]
	s_andn2_b64 s[10:11], s[74:75], exec
	s_and_b64 s[50:51], s[82:83], exec
	s_or_b64 s[74:75], s[10:11], s[50:51]
	s_andn2_b64 s[10:11], s[72:73], exec
	s_and_b64 s[50:51], s[86:87], exec
	s_or_b64 s[72:73], s[10:11], s[50:51]
	s_andn2_b64 s[10:11], s[70:71], exec
	s_and_b64 s[4:5], s[4:5], exec
	s_or_b64 s[70:71], s[10:11], s[4:5]
	s_andn2_b64 s[4:5], s[68:69], exec
	s_and_b64 s[10:11], s[94:95], exec
	s_or_b64 s[68:69], s[4:5], s[10:11]
	s_andn2_b64 s[4:5], s[66:67], exec
	s_and_b64 s[10:11], s[92:93], exec
	s_or_b64 s[66:67], s[4:5], s[10:11]
	s_andn2_b64 s[4:5], s[64:65], exec
	s_and_b64 s[10:11], s[90:91], exec
	s_or_b64 s[64:65], s[4:5], s[10:11]
	s_andn2_b64 s[4:5], s[62:63], exec
	s_and_b64 s[10:11], s[88:89], exec
	s_or_b64 s[62:63], s[4:5], s[10:11]
	s_andn2_b64 s[4:5], s[60:61], exec
	s_and_b64 s[10:11], s[96:97], exec
	s_or_b64 s[60:61], s[4:5], s[10:11]
	s_andn2_b64 s[4:5], s[58:59], exec
	s_and_b64 s[10:11], s[84:85], exec
	s_or_b64 s[58:59], s[4:5], s[10:11]
	s_andn2_b64 s[4:5], s[56:57], exec
	s_and_b64 s[8:9], s[8:9], exec
	s_or_b64 s[56:57], s[4:5], s[8:9]
	s_andn2_b64 s[4:5], s[54:55], exec
	s_and_b64 s[2:3], s[2:3], exec
	s_or_b64 s[54:55], s[4:5], s[2:3]
	s_andn2_b64 s[2:3], s[52:53], exec
	s_and_b64 s[4:5], s[6:7], exec
	s_or_b64 s[52:53], s[2:3], s[4:5]
	v_readlane_b32 s2, v116, 20
	v_readlane_b32 s4, v116, 22
	v_readlane_b32 s3, v116, 21
	v_readlane_b32 s5, v116, 23
	s_andn2_b64 s[2:3], s[2:3], exec
	s_and_b64 s[4:5], s[4:5], exec
	s_or_b64 s[2:3], s[2:3], s[4:5]
	v_writelane_b32 v116, s2, 20
	s_and_b64 s[0:1], s[0:1], exec
	s_andn2_b64 s[46:47], s[46:47], exec
	v_writelane_b32 v116, s3, 21
	s_andn2_b64 s[2:3], s[48:49], exec
	s_or_b64 s[48:49], s[2:3], s[0:1]
.Lwqd_166:
	v_readlane_b32 s0, v116, 16
	v_readlane_b32 s1, v116, 17
	s_or_b64 exec, exec, s[0:1]
	s_add_i32 s33, s33, 32
	s_and_b64 s[0:1], exec, s[48:49]
	s_or_b64 s[12:13], s[0:1], s[12:13]
	s_andn2_b64 s[0:1], s[14:15], exec
	s_and_b64 s[2:3], s[78:79], exec
	s_or_b64 s[14:15], s[0:1], s[2:3]
	s_andn2_b64 s[0:1], s[16:17], exec
	s_and_b64 s[2:3], s[76:77], exec
	s_or_b64 s[16:17], s[0:1], s[2:3]
	s_andn2_b64 s[0:1], s[18:19], exec
	s_and_b64 s[2:3], s[74:75], exec
	s_or_b64 s[18:19], s[0:1], s[2:3]
	s_andn2_b64 s[0:1], s[20:21], exec
	s_and_b64 s[2:3], s[72:73], exec
	s_or_b64 s[20:21], s[0:1], s[2:3]
	s_andn2_b64 s[0:1], s[22:23], exec
	s_and_b64 s[2:3], s[70:71], exec
	s_or_b64 s[22:23], s[0:1], s[2:3]
	s_andn2_b64 s[0:1], s[24:25], exec
	s_and_b64 s[2:3], s[68:69], exec
	s_or_b64 s[24:25], s[0:1], s[2:3]
	s_andn2_b64 s[0:1], s[26:27], exec
	s_and_b64 s[2:3], s[66:67], exec
	s_or_b64 s[26:27], s[0:1], s[2:3]
	s_andn2_b64 s[0:1], s[28:29], exec
	s_and_b64 s[2:3], s[64:65], exec
	s_or_b64 s[28:29], s[0:1], s[2:3]
	s_andn2_b64 s[0:1], s[30:31], exec
	s_and_b64 s[2:3], s[62:63], exec
	s_or_b64 s[30:31], s[0:1], s[2:3]
	s_andn2_b64 s[0:1], s[34:35], exec
	s_and_b64 s[2:3], s[60:61], exec
	s_or_b64 s[34:35], s[0:1], s[2:3]
	s_andn2_b64 s[0:1], s[36:37], exec
	s_and_b64 s[2:3], s[58:59], exec
	s_or_b64 s[36:37], s[0:1], s[2:3]
	s_andn2_b64 s[0:1], s[38:39], exec
	s_and_b64 s[2:3], s[56:57], exec
	s_or_b64 s[38:39], s[0:1], s[2:3]
	s_andn2_b64 s[0:1], s[40:41], exec
	s_and_b64 s[2:3], s[54:55], exec
	s_or_b64 s[40:41], s[0:1], s[2:3]
	s_andn2_b64 s[0:1], s[42:43], exec
	s_and_b64 s[2:3], s[52:53], exec
	s_or_b64 s[42:43], s[0:1], s[2:3]
	s_andn2_b64 s[0:1], s[44:45], exec
	s_and_b64 s[2:3], s[46:47], exec
	s_or_b64 s[44:45], s[0:1], s[2:3]
	v_readlane_b32 s0, v116, 14
	v_readlane_b32 s2, v116, 20
	v_readlane_b32 s1, v116, 15
	v_readlane_b32 s3, v116, 21
	s_andn2_b64 s[0:1], s[0:1], exec
	s_and_b64 s[2:3], s[2:3], exec
	v_mov_b32_e32 v44, s33
	s_or_b64 s[50:51], s[0:1], s[2:3]
	s_andn2_b64 exec, exec, s[12:13]
	s_cbranch_execz .Lwqd_183
.Lwqd_167:
	v_writelane_b32 v116, s50, 14
	s_movk_i32 s2, 0x84
	v_mov_b64_e32 v[64:65], v[70:71]
	v_writelane_b32 v116, s51, 15
	v_max_f32_e32 v48, v64, v64
	v_readlane_b32 s0, v116, 10
	s_andn2_b64 s[78:79], s[78:79], exec
	s_andn2_b64 s[76:77], s[76:77], exec
	v_add_u32_e32 v0, s0, v1
	v_readlane_b32 s0, v116, 12
	s_andn2_b64 s[74:75], s[74:75], exec
	s_andn2_b64 s[72:73], s[72:73], exec
	v_add_u32_e32 v44, s0, v8
	v_mad_u64_u32 v[46:47], s[0:1], v0, s2, v[4:5]
	ds_read_b32 v0, v46
	v_mad_u64_u32 v[46:47], s[0:1], v44, s2, v[4:5]
	ds_read_b32 v44, v46
	v_max_f32_e32 v47, v65, v65
	s_waitcnt lgkmcnt(1)
	v_cmp_u_f32_e32 vcc, v0, v0
	v_max_f32_e64 v46, |v0|, |v0|
	v_max_f32_e32 v47, v47, v46
	v_cndmask_b32_e64 v0, 0, 1, vcc
	s_waitcnt lgkmcnt(0)
	v_cmp_u_f32_e32 vcc, v44, v44
	v_max_f32_e64 v46, |v44|, |v44|
	v_lshlrev_b16_e32 v0, 1, v0
	v_cndmask_b32_e64 v44, 0, 1, vcc
	v_max_f32_e32 v46, v48, v46
	v_bitop3_b16 v0, v44, 3, v0 bitop3:0xc8
	s_andn2_b64 s[70:71], s[70:71], exec
	s_andn2_b64 s[68:69], s[68:69], exec
	s_andn2_b64 s[66:67], s[66:67], exec
	s_andn2_b64 s[64:65], s[64:65], exec
	s_andn2_b64 s[62:63], s[62:63], exec
	s_andn2_b64 s[60:61], s[60:61], exec
	s_andn2_b64 s[58:59], s[58:59], exec
	s_andn2_b64 s[56:57], s[56:57], exec
	s_andn2_b64 s[54:55], s[54:55], exec
	s_andn2_b64 s[52:53], s[52:53], exec
	s_or_b64 s[46:47], s[46:47], exec
	s_or_b64 s[48:49], s[48:49], exec
	v_cmp_eq_u16_e32 vcc, 0, v0
	s_mov_b64 s[0:1], exec
	v_writelane_b32 v116, s0, 16
	s_nop 1
	v_writelane_b32 v116, s1, 17
	s_and_b64 s[0:1], s[0:1], vcc
	s_mov_b64 exec, s[0:1]
	s_cbranch_execz .Lwqd_166
	v_readlane_b32 s0, v116, 10
	v_max_f32_e32 v52, v46, v46
	s_mov_b64 s[6:7], -1
	v_add_u32_e32 v0, s0, v5
	v_readlane_b32 s0, v116, 12
	s_mov_b64 s[8:9], 0
	s_mov_b64 s[84:85], 0
	v_add_u32_e32 v44, s0, v10
	v_mad_u64_u32 v[48:49], s[0:1], v0, s2, v[4:5]
	ds_read_b32 v0, v48
	v_mad_u64_u32 v[48:49], s[0:1], v44, s2, v[4:5]
	ds_read_b32 v44, v48
	v_max_f32_e32 v49, v47, v47
	s_waitcnt lgkmcnt(1)
	v_cmp_u_f32_e32 vcc, v0, v0
	v_max_f32_e64 v48, |v0|, |v0|
	v_max_f32_e32 v49, v49, v48
	v_cndmask_b32_e64 v0, 0, 1, vcc
	s_waitcnt lgkmcnt(0)
	v_cmp_u_f32_e32 vcc, v44, v44
	v_max_f32_e64 v48, |v44|, |v44|
	v_lshlrev_b16_e32 v0, 1, v0
	v_cndmask_b32_e64 v44, 0, 1, vcc
	v_max_f32_e32 v48, v52, v48
	v_bitop3_b16 v0, v44, 3, v0 bitop3:0xc8
	s_mov_b64 s[0:1], -1
	s_mov_b64 s[2:3], 0
	s_mov_b64 s[96:97], 0
	s_mov_b64 s[88:89], 0
	s_mov_b64 s[90:91], 0
	s_mov_b64 s[92:93], 0
	s_mov_b64 s[94:95], 0
	s_mov_b64 s[4:5], 0
	s_mov_b64 s[86:87], 0
	s_mov_b64 s[82:83], 0
	s_mov_b64 s[50:51], 0
	s_mov_b64 s[10:11], 0
	v_cmp_eq_u16_e32 vcc, 0, v0
	s_mov_b64 s[80:81], exec
	v_writelane_b32 v116, s80, 18
	s_and_b64 vcc, s[80:81], vcc
	s_nop 0
	v_writelane_b32 v116, s81, 19
	s_mov_b64 exec, vcc
	s_cbranch_execz .Lwqd_165
	v_readlane_b32 s0, v116, 10
	s_movk_i32 s2, 0x84
	v_max_f32_e32 v54, v48, v48
	v_add_u32_e32 v0, s0, v7
	v_readlane_b32 s0, v116, 12
	s_mov_b64 s[4:5], 0
	s_nop 0
	v_add_u32_e32 v44, s0, v12
	v_mad_u64_u32 v[52:53], s[0:1], v0, s2, v[4:5]
	ds_read_b32 v0, v52
	v_mad_u64_u32 v[52:53], s[0:1], v44, s2, v[4:5]
	ds_read_b32 v44, v52
	v_max_f32_e32 v53, v49, v49
	s_waitcnt lgkmcnt(1)
	v_cmp_u_f32_e32 vcc, v0, v0
	v_max_f32_e64 v52, |v0|, |v0|
	v_max_f32_e32 v53, v53, v52
	v_cndmask_b32_e64 v0, 0, 1, vcc
	s_waitcnt lgkmcnt(0)
	v_cmp_u_f32_e32 vcc, v44, v44
	v_max_f32_e64 v52, |v44|, |v44|
	v_lshlrev_b16_e32 v0, 1, v0
	v_cndmask_b32_e64 v44, 0, 1, vcc
	v_bitop3_b16 v0, v44, 3, v0 bitop3:0xc8
	v_max_f32_e32 v52, v54, v52
	v_cmp_eq_u16_e32 vcc, 0, v0
	s_mov_b64 s[0:1], -1
	s_mov_b64 s[2:3], 0
	s_and_saveexec_b64 s[80:81], vcc
	s_cbranch_execz .Lwqd_164
	v_readlane_b32 s0, v116, 10
	s_movk_i32 s2, 0x84
	v_max_f32_e32 v56, v52, v52
	v_add_u32_e32 v0, s0, v9
	v_readlane_b32 s0, v116, 12
	s_mov_b64 s[4:5], 0
	s_nop 0
	v_add_u32_e32 v44, s0, v14
	v_mad_u64_u32 v[54:55], s[0:1], v0, s2, v[4:5]
	ds_read_b32 v0, v54
	v_mad_u64_u32 v[54:55], s[0:1], v44, s2, v[4:5]
	ds_read_b32 v44, v54
	v_max_f32_e32 v55, v53, v53
	s_waitcnt lgkmcnt(1)
	v_cmp_u_f32_e32 vcc, v0, v0
	v_max_f32_e64 v54, |v0|, |v0|
	v_max_f32_e32 v55, v55, v54
	v_cndmask_b32_e64 v0, 0, 1, vcc
	s_waitcnt lgkmcnt(0)
	v_cmp_u_f32_e32 vcc, v44, v44
	v_max_f32_e64 v54, |v44|, |v44|
	v_lshlrev_b16_e32 v0, 1, v0
	v_cndmask_b32_e64 v44, 0, 1, vcc
	v_bitop3_b16 v0, v44, 3, v0 bitop3:0xc8
	v_max_f32_e32 v54, v56, v54
	v_cmp_eq_u16_e32 vcc, 0, v0
	s_mov_b64 s[0:1], -1
	s_mov_b64 s[2:3], 0
	s_and_saveexec_b64 s[96:97], vcc
	s_cbranch_execz .Lwqd_163
	v_readlane_b32 s0, v116, 10
	s_movk_i32 s2, 0x84
	v_max_f32_e32 v58, v54, v54
	v_add_u32_e32 v0, s0, v11
	v_readlane_b32 s0, v116, 12
	s_nop 1
	v_add_u32_e32 v44, s0, v16
	v_mad_u64_u32 v[56:57], s[0:1], v0, s2, v[4:5]
	ds_read_b32 v0, v56
	v_mad_u64_u32 v[56:57], s[0:1], v44, s2, v[4:5]
	ds_read_b32 v44, v56
	v_max_f32_e32 v57, v55, v55
	s_waitcnt lgkmcnt(1)
	v_cmp_u_f32_e32 vcc, v0, v0
	v_max_f32_e64 v56, |v0|, |v0|
	v_max_f32_e32 v57, v57, v56
	v_cndmask_b32_e64 v0, 0, 1, vcc
	s_waitcnt lgkmcnt(0)
	v_cmp_u_f32_e32 vcc, v44, v44
	v_max_f32_e64 v56, |v44|, |v44|
	v_lshlrev_b16_e32 v0, 1, v0
	v_cndmask_b32_e64 v44, 0, 1, vcc
	v_bitop3_b16 v0, v44, 3, v0 bitop3:0xc8
	v_max_f32_e32 v56, v58, v56
	v_cmp_eq_u16_e32 vcc, 0, v0
	s_mov_b64 s[0:1], -1
	s_mov_b64 s[2:3], 0
	s_and_saveexec_b64 s[8:9], vcc
	s_cbranch_execz .Lwqd_162
	v_readlane_b32 s0, v116, 10
	s_movk_i32 s2, 0x84
	v_max_f32_e32 v60, v56, v56
	v_add_u32_e32 v0, s0, v13
	v_readlane_b32 s0, v116, 12
	s_mov_b64 s[4:5], -1
	s_nop 0
	v_add_u32_e32 v44, s0, v18
	v_mad_u64_u32 v[58:59], s[0:1], v0, s2, v[4:5]
	ds_read_b32 v0, v58
	v_mad_u64_u32 v[58:59], s[0:1], v44, s2, v[4:5]
	ds_read_b32 v44, v58
	v_max_f32_e32 v59, v57, v57
	s_waitcnt lgkmcnt(1)
	v_cmp_u_f32_e32 vcc, v0, v0
	v_max_f32_e64 v58, |v0|, |v0|
	v_max_f32_e32 v59, v59, v58
	v_cndmask_b32_e64 v0, 0, 1, vcc
	s_waitcnt lgkmcnt(0)
	v_cmp_u_f32_e32 vcc, v44, v44
	v_max_f32_e64 v58, |v44|, |v44|
	v_lshlrev_b16_e32 v0, 1, v0
	v_cndmask_b32_e64 v44, 0, 1, vcc
	v_bitop3_b16 v0, v44, 3, v0 bitop3:0xc8
	v_max_f32_e32 v58, v60, v58
	v_cmp_eq_u16_e32 vcc, 0, v0
	s_mov_b64 s[2:3], 0
	s_and_saveexec_b64 s[0:1], vcc
	s_cbranch_execz .Lwqd_161
	v_readlane_b32 s2, v116, 10
	s_movk_i32 s4, 0x84
	v_max_f32_e32 v62, v58, v58
	v_add_u32_e32 v0, s2, v15
	v_readlane_b32 s2, v116, 12
	s_mov_b64 s[84:85], -1
	s_nop 0
	v_add_u32_e32 v44, s2, v20
	v_mad_u64_u32 v[60:61], s[2:3], v0, s4, v[4:5]
	ds_read_b32 v0, v60
	v_mad_u64_u32 v[60:61], s[2:3], v44, s4, v[4:5]
	ds_read_b32 v44, v60
	v_max_f32_e32 v61, v59, v59
	s_waitcnt lgkmcnt(1)
	v_cmp_u_f32_e32 vcc, v0, v0
	v_max_f32_e64 v60, |v0|, |v0|
	v_max_f32_e32 v61, v61, v60
	v_cndmask_b32_e64 v0, 0, 1, vcc
	s_waitcnt lgkmcnt(0)
	v_cmp_u_f32_e32 vcc, v44, v44
	v_max_f32_e64 v60, |v44|, |v44|
	v_lshlrev_b16_e32 v0, 1, v0
	v_cndmask_b32_e64 v44, 0, 1, vcc
	v_bitop3_b16 v0, v44, 3, v0 bitop3:0xc8
	v_max_f32_e32 v60, v62, v60
	v_cmp_eq_u16_e32 vcc, 0, v0
	s_mov_b64 s[4:5], -1
	s_mov_b64 s[2:3], 0
	s_and_saveexec_b64 s[6:7], vcc
	s_cbranch_execz .Lwqd_160
	v_readlane_b32 s2, v116, 10
	s_movk_i32 s4, 0x84
	v_max_f32_e32 v66, v60, v60
	v_add_u32_e32 v0, s2, v17
	v_readlane_b32 s2, v116, 12
	s_nop 1
	v_add_u32_e32 v44, s2, v22
	v_mad_u64_u32 v[62:63], s[2:3], v0, s4, v[4:5]
	ds_read_b32 v0, v62
	v_mad_u64_u32 v[62:63], s[2:3], v44, s4, v[4:5]
	ds_read_b32 v44, v62
	v_max_f32_e32 v63, v61, v61
	s_waitcnt lgkmcnt(1)
	v_cmp_u_f32_e32 vcc, v0, v0
	v_max_f32_e64 v62, |v0|, |v0|
	v_max_f32_e32 v63, v63, v62
	v_cndmask_b32_e64 v0, 0, 1, vcc
	s_waitcnt lgkmcnt(0)
	v_cmp_u_f32_e32 vcc, v44, v44
	v_max_f32_e64 v62, |v44|, |v44|
	v_lshlrev_b16_e32 v0, 1, v0
	v_cndmask_b32_e64 v44, 0, 1, vcc
	v_bitop3_b16 v0, v44, 3, v0 bitop3:0xc8
	v_max_f32_e32 v62, v66, v62
	v_cmp_eq_u16_e32 vcc, 0, v0
	s_mov_b64 s[4:5], -1
	s_and_saveexec_b64 s[2:3], vcc
	s_cbranch_execz .Lwqd_159
	v_readlane_b32 s4, v116, 10
	s_movk_i32 s10, 0x84
	v_max_f32_e32 v68, v62, v62
	v_add_u32_e32 v0, s4, v19
	v_readlane_b32 s4, v116, 12
	s_mov_b64 s[50:51], 0
	s_nop 0
	v_add_u32_e32 v44, s4, v24
	v_mad_u64_u32 v[66:67], s[4:5], v0, s10, v[4:5]
	ds_read_b32 v0, v66
	v_mad_u64_u32 v[66:67], s[4:5], v44, s10, v[4:5]
	ds_read_b32 v44, v66
	v_max_f32_e32 v67, v63, v63
	s_waitcnt lgkmcnt(1)
	v_cmp_u_f32_e32 vcc, v0, v0
	v_max_f32_e64 v66, |v0|, |v0|
	v_max_f32_e32 v67, v67, v66
	v_cndmask_b32_e64 v0, 0, 1, vcc
	s_waitcnt lgkmcnt(0)
	v_cmp_u_f32_e32 vcc, v44, v44
	v_max_f32_e64 v66, |v44|, |v44|
	v_lshlrev_b16_e32 v0, 1, v0
	v_cndmask_b32_e64 v44, 0, 1, vcc
	v_bitop3_b16 v0, v44, 3, v0 bitop3:0xc8
	v_max_f32_e32 v66, v68, v66
	v_cmp_eq_u16_e32 vcc, 0, v0
	s_mov_b64 s[4:5], -1
	s_mov_b64 s[10:11], 0
	s_and_saveexec_b64 s[94:95], vcc
	s_cbranch_execz .Lwqd_158
	v_readlane_b32 s4, v116, 10
	s_movk_i32 s10, 0x84
	v_max_f32_e32 v70, v66, v66
	v_add_u32_e32 v0, s4, v21
	v_readlane_b32 s4, v116, 12
	s_mov_b64 s[50:51], 0
	s_nop 0
	v_add_u32_e32 v44, s4, v26
	v_mad_u64_u32 v[68:69], s[4:5], v0, s10, v[4:5]
	ds_read_b32 v0, v68
	v_mad_u64_u32 v[68:69], s[4:5], v44, s10, v[4:5]
	ds_read_b32 v44, v68
	v_max_f32_e32 v69, v67, v67
	s_waitcnt lgkmcnt(1)
	v_cmp_u_f32_e32 vcc, v0, v0
	v_max_f32_e64 v68, |v0|, |v0|
	v_max_f32_e32 v69, v69, v68
	v_cndmask_b32_e64 v0, 0, 1, vcc
	s_waitcnt lgkmcnt(0)
	v_cmp_u_f32_e32 vcc, v44, v44
	v_max_f32_e64 v68, |v44|, |v44|
	v_lshlrev_b16_e32 v0, 1, v0
	v_cndmask_b32_e64 v44, 0, 1, vcc
	v_bitop3_b16 v0, v44, 3, v0 bitop3:0xc8
	v_max_f32_e32 v68, v70, v68
	v_cmp_eq_u16_e32 vcc, 0, v0
	s_mov_b64 s[4:5], -1
	s_mov_b64 s[10:11], 0
	s_and_saveexec_b64 s[92:93], vcc
	s_cbranch_execz .Lwqd_157
	v_readlane_b32 s4, v116, 10
	s_movk_i32 s10, 0x84
	s_mov_b64 s[50:51], 0
	v_add_u32_e32 v0, s4, v23
	v_readlane_b32 s4, v116, 12
	s_nop 1
	v_add_u32_e32 v44, s4, v28
	v_mad_u64_u32 v[70:71], s[4:5], v0, s10, v[4:5]
	ds_read_b32 v0, v70
	v_mad_u64_u32 v[70:71], s[4:5], v44, s10, v[4:5]
	ds_read_b32 v44, v70
	v_max_f32_e32 v71, v69, v69
	s_waitcnt lgkmcnt(1)
	v_cmp_u_f32_e32 vcc, v0, v0
	v_max_f32_e64 v70, |v0|, |v0|
	v_max_f32_e32 v75, v71, v70
	v_cndmask_b32_e64 v0, 0, 1, vcc
	s_waitcnt lgkmcnt(0)
	v_cmp_u_f32_e32 vcc, v44, v44
	v_max_f32_e64 v70, |v44|, |v44|
	v_lshlrev_b16_e32 v0, 1, v0
	v_cndmask_b32_e64 v44, 0, 1, vcc
	v_max_f32_e32 v71, v68, v68
	v_bitop3_b16 v0, v44, 3, v0 bitop3:0xc8
	v_max_f32_e32 v74, v71, v70
	v_cmp_eq_u16_e32 vcc, 0, v0
	s_mov_b64 s[4:5], -1
	s_mov_b64 s[10:11], 0
	s_and_saveexec_b64 s[90:91], vcc
	s_cbranch_execz .Lwqd_156
	v_readlane_b32 s4, v116, 10
	s_movk_i32 s10, 0x84
	s_mov_b64 s[50:51], 0
	v_add_u32_e32 v0, s4, v25
	v_readlane_b32 s4, v116, 12
	s_nop 1
	v_add_u32_e32 v44, s4, v30
	v_mad_u64_u32 v[70:71], s[4:5], v0, s10, v[4:5]
	ds_read_b32 v0, v70
	v_mad_u64_u32 v[70:71], s[4:5], v44, s10, v[4:5]
	ds_read_b32 v44, v70
	v_max_f32_e32 v71, v75, v75
	s_waitcnt lgkmcnt(1)
	v_cmp_u_f32_e32 vcc, v0, v0
	v_max_f32_e64 v70, |v0|, |v0|
	v_max_f32_e32 v77, v71, v70
	v_cndmask_b32_e64 v0, 0, 1, vcc
	s_waitcnt lgkmcnt(0)
	v_cmp_u_f32_e32 vcc, v44, v44
	v_max_f32_e64 v70, |v44|, |v44|
	v_lshlrev_b16_e32 v0, 1, v0
	v_cndmask_b32_e64 v44, 0, 1, vcc
	v_max_f32_e32 v71, v74, v74
	v_bitop3_b16 v0, v44, 3, v0 bitop3:0xc8
	v_max_f32_e32 v76, v71, v70
	v_cmp_eq_u16_e32 vcc, 0, v0
	s_mov_b64 s[4:5], -1
	s_mov_b64 s[10:11], 0
	s_and_saveexec_b64 s[88:89], vcc
	s_cbranch_execz .Lwqd_155
	v_readlane_b32 s4, v116, 10
	s_movk_i32 s10, 0x84
	s_mov_b64 s[50:51], 0
	v_add_u32_e32 v0, s4, v27
	v_readlane_b32 s4, v116, 12
	s_nop 1
	v_add_u32_e32 v44, s4, v32
	v_mad_u64_u32 v[70:71], s[4:5], v0, s10, v[4:5]
	ds_read_b32 v0, v70
	v_mad_u64_u32 v[70:71], s[4:5], v44, s10, v[4:5]
	ds_read_b32 v44, v70
	v_max_f32_e32 v71, v77, v77
	s_waitcnt lgkmcnt(1)
	v_cmp_u_f32_e32 vcc, v0, v0
	v_max_f32_e64 v70, |v0|, |v0|
	v_max_f32_e32 v79, v71, v70
	v_cndmask_b32_e64 v0, 0, 1, vcc
	s_waitcnt lgkmcnt(0)
	v_cmp_u_f32_e32 vcc, v44, v44
	v_max_f32_e64 v70, |v44|, |v44|
	v_max_f32_e32 v71, v76, v76
	v_lshlrev_b16_e32 v0, 1, v0
	v_cndmask_b32_e64 v44, 0, 1, vcc
	v_max_f32_e32 v78, v71, v70
	v_bitop3_b16 v0, v44, 3, v0 bitop3:0xc8
	s_mov_b64 s[4:5], -1
	s_mov_b64 s[10:11], 0
	v_cmp_eq_u16_e32 vcc, 0, v0
	s_mov_b64 s[82:83], exec
	v_writelane_b32 v116, s82, 24
	s_nop 1
	v_writelane_b32 v116, s83, 25
	s_and_b64 s[82:83], s[82:83], vcc
	s_mov_b64 exec, s[82:83]
	s_cbranch_execz .Lwqd_154
	v_readlane_b32 s4, v116, 10
	s_movk_i32 s10, 0x84
	s_mov_b64 s[82:83], -1
	v_add_u32_e32 v0, s4, v29
	v_readlane_b32 s4, v116, 12
	s_nop 1
	v_add_u32_e32 v44, s4, v34
	v_mad_u64_u32 v[70:71], s[4:5], v0, s10, v[4:5]
	ds_read_b32 v0, v70
	v_mad_u64_u32 v[70:71], s[4:5], v44, s10, v[4:5]
	ds_read_b32 v44, v70
	v_max_f32_e32 v71, v79, v79
	s_waitcnt lgkmcnt(1)
	v_cmp_u_f32_e32 vcc, v0, v0
	v_max_f32_e64 v70, |v0|, |v0|
	v_max_f32_e32 v81, v71, v70
	v_cndmask_b32_e64 v0, 0, 1, vcc
	s_waitcnt lgkmcnt(0)
	v_cmp_u_f32_e32 vcc, v44, v44
	v_max_f32_e64 v70, |v44|, |v44|
	v_lshlrev_b16_e32 v0, 1, v0
	v_cndmask_b32_e64 v44, 0, 1, vcc
	v_max_f32_e32 v71, v78, v78
	v_bitop3_b16 v0, v44, 3, v0 bitop3:0xc8
	v_max_f32_e32 v80, v71, v70
	v_cmp_eq_u16_e32 vcc, 0, v0
	s_mov_b64 s[10:11], 0
	s_and_saveexec_b64 s[4:5], vcc
	s_cbranch_execz .Lwqd_153
	v_readlane_b32 s10, v116, 10
	s_movk_i32 s50, 0x84
	s_nop 0
	v_add_u32_e32 v0, s10, v31
	v_readlane_b32 s10, v116, 12
	s_nop 1
	v_add_u32_e32 v44, s10, v36
	v_mad_u64_u32 v[70:71], s[10:11], v0, s50, v[4:5]
	ds_read_b32 v0, v70
	v_mad_u64_u32 v[70:71], s[10:11], v44, s50, v[4:5]
	ds_read_b32 v44, v70
	v_max_f32_e32 v71, v81, v81
	s_waitcnt lgkmcnt(1)
	v_cmp_u_f32_e32 vcc, v0, v0
	v_max_f32_e64 v70, |v0|, |v0|
	v_max_f32_e32 v73, v71, v70
	v_cndmask_b32_e64 v0, 0, 1, vcc
	s_waitcnt lgkmcnt(0)
	v_cmp_u_f32_e32 vcc, v44, v44
	v_max_f32_e64 v70, |v44|, |v44|
	v_lshlrev_b16_e32 v0, 1, v0
	v_cndmask_b32_e64 v44, 0, 1, vcc
	v_max_f32_e32 v71, v80, v80
	v_bitop3_b16 v0, v44, 3, v0 bitop3:0xc8
	v_max_f32_e32 v72, v71, v70
	v_cmp_eq_u16_e32 vcc, 0, v0
	s_mov_b64 s[50:51], -1
	s_and_saveexec_b64 s[10:11], vcc
	s_cbranch_execz .Lwqd_152
	v_readlane_b32 s83, v116, 10
	v_readlane_b32 s84, v116, 12
	s_movk_i32 s82, 0x84
	v_add_u32_e32 v0, s83, v33
	v_add_u32_e32 v44, s84, v38
	v_mad_u64_u32 v[70:71], s[50:51], v0, s82, v[4:5]
	ds_read_b32 v0, v70
	v_mad_u64_u32 v[70:71], s[50:51], v44, s82, v[4:5]
	ds_read_b32 v44, v70
	v_max_f32_e32 v71, v73, v73
	s_waitcnt lgkmcnt(1)
	v_cmp_u_f32_e32 vcc, v0, v0
	v_max_f32_e64 v70, |v0|, |v0|
	v_max_f32_e32 v71, v71, v70
	v_cndmask_b32_e64 v0, 0, 1, vcc
	s_waitcnt lgkmcnt(0)
	v_cmp_u_f32_e32 vcc, v44, v44
	v_max_f32_e64 v70, |v44|, |v44|
	v_lshlrev_b16_e32 v0, 1, v0
	v_cndmask_b32_e64 v44, 0, 1, vcc
	s_cmp_eq_u32 s33, 0
	v_bitop3_b16 v0, v44, 3, v0 bitop3:0xc8
	s_cselect_b64 s[50:51], -1, 0
	v_cmp_ne_u16_e64 s[86:87], 0, v0
	s_add_i32 s84, s84, 32
	v_max_f32_e32 v87, v72, v72
	v_writelane_b32 v116, s86, 22
	s_or_b64 s[50:51], s[86:87], s[50:51]
	v_writelane_b32 v116, s84, 12
	s_add_i32 s83, s83, 32
	v_max_f32_e32 v70, v87, v70
	v_writelane_b32 v116, s87, 23
	v_writelane_b32 v116, s83, 10
	s_xor_b64 s[82:83], exec, -1
	s_orn2_b64 s[50:51], s[50:51], exec
	s_branch .Lwqd_152
.Lwqd_183:
	s_or_b64 exec, exec, s[12:13]
	s_mov_b64 s[2:3], -1
	s_xor_b64 s[0:1], s[44:45], -1
	s_xor_b64 s[44:45], s[42:43], -1
	s_xor_b64 s[6:7], s[40:41], -1
	s_xor_b64 s[8:9], s[38:39], -1
	s_xor_b64 s[12:13], s[36:37], -1
	s_xor_b64 s[42:43], s[34:35], -1
	s_xor_b64 s[40:41], s[30:31], -1
	s_xor_b64 s[38:39], s[28:29], -1
	s_xor_b64 s[36:37], s[26:27], -1
	s_xor_b64 s[10:11], s[24:25], -1
	s_xor_b64 s[4:5], s[22:23], -1
	s_xor_b64 s[34:35], s[20:21], -1
	s_xor_b64 s[30:31], s[18:19], -1
	s_xor_b64 s[28:29], s[16:17], -1
	s_xor_b64 s[26:27], s[14:15], -1
	s_and_saveexec_b64 s[14:15], s[0:1]
	v_readlane_b32 s52, v252, 26
	s_xor_b64 s[0:1], exec, s[14:15]
	v_readlane_b32 s53, v252, 27
	v_readlane_b32 s56, v252, 30
	v_readlane_b32 s57, v252, 31
	v_readlane_b32 s33, v116, 8
	v_readlane_b32 s54, v252, 28
	v_readlane_b32 s55, v252, 29
	v_readlane_b32 s58, v252, 32
	v_readlane_b32 s59, v252, 33
	v_readlane_b32 s60, v252, 34
	v_readlane_b32 s61, v252, 35
	v_readlane_b32 s62, v252, 36
	v_readlane_b32 s63, v252, 37
	v_readlane_b32 s64, v252, 38
	v_readlane_b32 s65, v252, 39
	v_readlane_b32 s66, v252, 40
	v_readlane_b32 s67, v252, 41
	s_cbranch_execz .Lwqd_241
	s_and_saveexec_b64 s[2:3], s[44:45]
	s_xor_b64 s[2:3], exec, s[2:3]
	s_cbranch_execz .Lwqd_238
	s_and_saveexec_b64 s[14:15], s[6:7]
	s_xor_b64 s[6:7], exec, s[14:15]
	s_cbranch_execz .Lwqd_235
	s_and_saveexec_b64 s[14:15], s[8:9]
	s_xor_b64 s[8:9], exec, s[14:15]
	s_cbranch_execz .Lwqd_232
	s_and_saveexec_b64 s[14:15], s[12:13]
	s_xor_b64 s[12:13], exec, s[14:15]
	s_cbranch_execz .Lwqd_229
	s_and_saveexec_b64 s[14:15], s[42:43]
	s_xor_b64 s[14:15], exec, s[14:15]
	s_cbranch_execz .Lwqd_226
	s_and_saveexec_b64 s[16:17], s[40:41]
	s_xor_b64 s[16:17], exec, s[16:17]
	s_cbranch_execz .Lwqd_223
	s_and_saveexec_b64 s[18:19], s[38:39]
	s_xor_b64 s[18:19], exec, s[18:19]
	s_cbranch_execz .Lwqd_220
	s_and_saveexec_b64 s[20:21], s[36:37]
	s_xor_b64 s[20:21], exec, s[20:21]
	s_cbranch_execz .Lwqd_217
	s_and_saveexec_b64 s[22:23], s[10:11]
	s_xor_b64 s[22:23], exec, s[22:23]
	s_cbranch_execz .Lwqd_214
	s_and_saveexec_b64 s[10:11], s[4:5]
	s_xor_b64 s[24:25], exec, s[10:11]
	s_cbranch_execz .Lwqd_211
	s_and_saveexec_b64 s[4:5], s[34:35]
	s_xor_b64 s[34:35], exec, s[4:5]
	s_cbranch_execz .Lwqd_208
	s_and_saveexec_b64 s[4:5], s[30:31]
	s_xor_b64 s[4:5], exec, s[4:5]
	s_cbranch_execz .Lwqd_205
	s_and_saveexec_b64 s[10:11], s[28:29]
	s_xor_b64 s[10:11], exec, s[10:11]
	s_cbranch_execz .Lwqd_202
	s_and_saveexec_b64 s[28:29], s[26:27]
	s_xor_b64 s[26:27], exec, s[28:29]
	v_or_b32_e32 v64, 30, v44
	s_andn2_saveexec_b64 s[26:27], s[26:27]
	v_or_b32_e32 v64, 28, v44
	s_or_b64 s[50:51], s[50:51], exec
	v_mov_b64_e32 v[70:71], v[72:73]
	v_mov_b64_e32 v[72:73], v[80:81]
	s_or_b64 exec, exec, s[26:27]

.Lwqd_251:
	s_or_b64 exec, exec, s[0:1]
	ds_write_b32 v39, v48
	s_waitcnt lgkmcnt(0)
	s_barrier
	s_mov_b64 s[0:1], exec
	v_readlane_b32 s2, v116, 0
	v_readlane_b32 s3, v116, 1
	s_and_b64 s[2:3], s[0:1], s[2:3]
	s_mov_b64 exec, s[2:3]
	s_cbranch_execz .Lwqd_111
	ds_read2_b32 v[46:47], v39 offset1:32
	ds_read2_b32 v[48:49], v39 offset0:64 offset1:96
	ds_read2_b32 v[52:53], v39 offset0:128 offset1:160
	ds_read2_b32 v[54:55], v39 offset0:192 offset1:224
	v_readlane_b32 s2, v116, 6
	s_waitcnt lgkmcnt(3)
	v_max_f32_e32 v0, v47, v47
	v_max_f32_e32 v44, v46, v46
	v_max_f32_e32 v0, v44, v0
	s_waitcnt lgkmcnt(2)
	v_max3_f32 v0, v0, v48, v49
	v_add_u32_e32 v44, 0x400, v39
	s_waitcnt lgkmcnt(1)
	v_max3_f32 v0, v0, v52, v53
	ds_read2_b32 v[46:47], v44 offset1:32
	ds_read2_b32 v[48:49], v44 offset0:64 offset1:96
	ds_read2_b32 v[52:53], v44 offset0:128 offset1:160
	ds_read2_b32 v[56:57], v44 offset0:192 offset1:224
	s_waitcnt lgkmcnt(4)
	v_max3_f32 v0, v0, v54, v55
	s_waitcnt lgkmcnt(3)
	v_max3_f32 v0, v0, v46, v47
	s_waitcnt lgkmcnt(2)
	v_max3_f32 v0, v0, v48, v49
	s_waitcnt lgkmcnt(1)
	v_max3_f32 v0, v0, v52, v53
	v_add_u32_e32 v46, s33, v50
	s_waitcnt lgkmcnt(0)
	v_max3_f32 v0, v0, v56, v57
	v_ashrrev_i32_e32 v47, 31, v46
	v_readlane_b32 s3, v116, 7
	ds_write_b32 v43, v0
	v_mul_f32_e32 v0, 0x3c010204, v0
	v_lshl_add_u64 v[46:47], v[46:47], 2, s[2:3]
	global_store_dword v[46:47], v0, off
	s_branch .Lwqd_111
.Lwqd_exit:
	s_mov_b64 exec, -1
	s_cmp_eq_u32 s101, 1
	s_cbranch_scc1 .Lwqd_ret_A
	s_cmp_eq_u32 s101, 2
	s_endpgm

.LBB0_1159:
	v_readlane_b32 s98, v251, 3
	v_readlane_b32 s99, v255, 29
	s_cmp_lt_u32 s98, 16
	s_cbranch_scc1 .Lwqd_skip_A
	s_sub_i32 s98, s98, 16
	s_mov_b32 s100, 0
	s_mov_b32 s101, 0
	s_cmp_eq_u32 s99, 0
	s_cselect_b32 s100, 0xdc0, s100
	s_cselect_b32 s101, 0xfa0, s101
	s_cmp_eq_u32 s99, 1
	s_cselect_b32 s100, 0xfa0, s100
	s_cselect_b32 s101, 0x1180, s101
	s_cmp_eq_u32 s99, 2
	s_cselect_b32 s100, 0x1180, s100
	s_cselect_b32 s101, 0x1360, s101
	s_add_i32 s98, s98, s100
	s_mov_b32 s99, s101
	s_cmp_ge_u32 s98, s99
	s_cbranch_scc1 .Lwqd_skip_A
	s_movk_i32 s100, 240
	s_mov_b32 s101, 1
	v_writelane_b32 v117, s0, 0
	v_writelane_b32 v117, s1, 1
	v_writelane_b32 v117, s2, 2
	v_writelane_b32 v117, s3, 3
	v_writelane_b32 v117, s4, 4
	v_writelane_b32 v117, s5, 5
	v_writelane_b32 v117, s6, 6
	v_writelane_b32 v117, s7, 7
	v_writelane_b32 v117, s8, 8
	v_writelane_b32 v117, s9, 9
	v_writelane_b32 v117, s10, 10
	v_writelane_b32 v117, s11, 11
	v_writelane_b32 v117, s12, 12
	v_writelane_b32 v117, s13, 13
	v_writelane_b32 v117, s14, 14
	v_writelane_b32 v117, s15, 15
	v_writelane_b32 v117, s16, 16
	v_writelane_b32 v117, s17, 17
	v_writelane_b32 v117, s18, 18
	v_writelane_b32 v117, s19, 19
	v_writelane_b32 v117, s20, 20
	v_writelane_b32 v117, s21, 21
	v_writelane_b32 v117, s22, 22
	v_writelane_b32 v117, s23, 23
	v_writelane_b32 v117, s24, 24
	v_writelane_b32 v117, s25, 25
	v_writelane_b32 v117, s26, 26
	v_writelane_b32 v117, s27, 27
	v_writelane_b32 v117, s28, 28
	v_writelane_b32 v117, s29, 29
	v_writelane_b32 v117, s30, 30
	v_writelane_b32 v117, s31, 31
	v_writelane_b32 v117, s32, 32
	v_writelane_b32 v117, s33, 33
	v_writelane_b32 v117, s34, 34
	v_writelane_b32 v117, s35, 35
	v_writelane_b32 v117, s36, 36
	v_writelane_b32 v117, s37, 37
	v_writelane_b32 v117, s38, 38
	v_writelane_b32 v117, s39, 39
	v_writelane_b32 v117, s40, 40
	v_writelane_b32 v117, s41, 41
	v_writelane_b32 v117, s42, 42
	v_writelane_b32 v117, s43, 43
	v_writelane_b32 v117, s44, 44
	v_writelane_b32 v117, s45, 45
	v_writelane_b32 v117, s46, 46
	v_writelane_b32 v117, s47, 47
	v_writelane_b32 v117, s48, 48
	v_writelane_b32 v117, s49, 49
	v_writelane_b32 v117, s50, 50
	v_writelane_b32 v117, s51, 51
	v_writelane_b32 v117, s52, 52
	v_writelane_b32 v117, s53, 53
	v_writelane_b32 v117, s54, 54
	v_writelane_b32 v117, s55, 55
	v_writelane_b32 v117, s56, 56
	v_writelane_b32 v117, s57, 57
	v_writelane_b32 v117, s58, 58
	v_writelane_b32 v117, s59, 59
	v_writelane_b32 v117, s60, 60
	v_writelane_b32 v117, s61, 61
	v_writelane_b32 v117, s62, 62
	v_writelane_b32 v117, s63, 63
	v_writelane_b32 v118, s64, 0
	v_writelane_b32 v118, s65, 1
	v_writelane_b32 v118, s66, 2
	v_writelane_b32 v118, s67, 3
	v_writelane_b32 v118, s68, 4
	v_writelane_b32 v118, s69, 5
	v_writelane_b32 v118, s70, 6
	v_writelane_b32 v118, s71, 7
	v_writelane_b32 v118, s72, 8
	v_writelane_b32 v118, s73, 9
	v_writelane_b32 v118, s74, 10
	v_writelane_b32 v118, s75, 11
	v_writelane_b32 v118, s76, 12
	v_writelane_b32 v118, s77, 13
	v_writelane_b32 v118, s78, 14
	v_writelane_b32 v118, s79, 15
	v_writelane_b32 v118, s80, 16
	v_writelane_b32 v118, s81, 17
	v_writelane_b32 v118, s82, 18
	v_writelane_b32 v118, s83, 19
	v_writelane_b32 v118, s84, 20
	v_writelane_b32 v118, s85, 21
	v_writelane_b32 v118, s86, 22
	v_writelane_b32 v118, s87, 23
	v_writelane_b32 v118, s88, 24
	v_writelane_b32 v118, s89, 25
	v_writelane_b32 v118, s90, 26
	v_writelane_b32 v118, s91, 27
	v_writelane_b32 v118, s92, 28
	v_writelane_b32 v118, s93, 29
	v_writelane_b32 v118, s94, 30
	v_writelane_b32 v118, s95, 31
	v_writelane_b32 v118, s96, 32
	v_writelane_b32 v118, s97, 33
	v_mov_b32_e32 v100, v0
	v_mov_b32_e32 v101, v50
	v_mov_b32_e32 v102, v51
	v_mov_b32_e32 v103, v52
	v_mov_b32_e32 v104, v54
	v_mov_b32_e32 v105, v55
	v_mov_b32_e32 v106, v56
	v_mov_b32_e32 v107, v58
	v_mov_b32_e32 v108, v59
	v_mov_b32_e32 v109, v60
	v_mov_b32_e32 v110, v62
	v_mov_b32_e32 v111, v63
	v_mov_b32_e32 v112, v64
	v_mov_b32_e32 v113, v67
	v_mov_b32_e32 v114, v75
	v_mov_b32_e32 v115, v77
	s_branch .Lwqd_entry
.Lwqd_ret_A:
	v_mov_b32_e32 v0, v100
	v_mov_b32_e32 v50, v101
	v_mov_b32_e32 v51, v102
	v_mov_b32_e32 v52, v103
	v_mov_b32_e32 v54, v104
	v_mov_b32_e32 v55, v105
	v_mov_b32_e32 v56, v106
	v_mov_b32_e32 v58, v107
	v_mov_b32_e32 v59, v108
	v_mov_b32_e32 v60, v109
	v_mov_b32_e32 v62, v110
	v_mov_b32_e32 v63, v111
	v_mov_b32_e32 v64, v112
	v_mov_b32_e32 v67, v113
	v_mov_b32_e32 v75, v114
	v_mov_b32_e32 v77, v115
	v_readlane_b32 s0, v117, 0
	v_readlane_b32 s1, v117, 1
	v_readlane_b32 s2, v117, 2
	v_readlane_b32 s3, v117, 3
	v_readlane_b32 s4, v117, 4
	v_readlane_b32 s5, v117, 5
	v_readlane_b32 s6, v117, 6
	v_readlane_b32 s7, v117, 7
	v_readlane_b32 s8, v117, 8
	v_readlane_b32 s9, v117, 9
	v_readlane_b32 s10, v117, 10
	v_readlane_b32 s11, v117, 11
	v_readlane_b32 s12, v117, 12
	v_readlane_b32 s13, v117, 13
	v_readlane_b32 s14, v117, 14
	v_readlane_b32 s15, v117, 15
	v_readlane_b32 s16, v117, 16
	v_readlane_b32 s17, v117, 17
	v_readlane_b32 s18, v117, 18
	v_readlane_b32 s19, v117, 19
	v_readlane_b32 s20, v117, 20
	v_readlane_b32 s21, v117, 21
	v_readlane_b32 s22, v117, 22
	v_readlane_b32 s23, v117, 23
	v_readlane_b32 s24, v117, 24
	v_readlane_b32 s25, v117, 25
	v_readlane_b32 s26, v117, 26
	v_readlane_b32 s27, v117, 27
	v_readlane_b32 s28, v117, 28
	v_readlane_b32 s29, v117, 29
	v_readlane_b32 s30, v117, 30
	v_readlane_b32 s31, v117, 31
	v_readlane_b32 s32, v117, 32
	v_readlane_b32 s33, v117, 33
	v_readlane_b32 s34, v117, 34
	v_readlane_b32 s35, v117, 35
	v_readlane_b32 s36, v117, 36
	v_readlane_b32 s37, v117, 37
	v_readlane_b32 s38, v117, 38
	v_readlane_b32 s39, v117, 39
	v_readlane_b32 s40, v117, 40
	v_readlane_b32 s41, v117, 41
	v_readlane_b32 s42, v117, 42
	v_readlane_b32 s43, v117, 43
	v_readlane_b32 s44, v117, 44
	v_readlane_b32 s45, v117, 45
	v_readlane_b32 s46, v117, 46
	v_readlane_b32 s47, v117, 47
	v_readlane_b32 s48, v117, 48
	v_readlane_b32 s49, v117, 49
	v_readlane_b32 s50, v117, 50
	v_readlane_b32 s51, v117, 51
	v_readlane_b32 s52, v117, 52
	v_readlane_b32 s53, v117, 53
	v_readlane_b32 s54, v117, 54
	v_readlane_b32 s55, v117, 55
	v_readlane_b32 s56, v117, 56
	v_readlane_b32 s57, v117, 57
	v_readlane_b32 s58, v117, 58
	v_readlane_b32 s59, v117, 59
	v_readlane_b32 s60, v117, 60
	v_readlane_b32 s61, v117, 61
	v_readlane_b32 s62, v117, 62
	v_readlane_b32 s63, v117, 63
	v_readlane_b32 s64, v118, 0
	v_readlane_b32 s65, v118, 1
	v_readlane_b32 s66, v118, 2
	v_readlane_b32 s67, v118, 3
	v_readlane_b32 s68, v118, 4
	v_readlane_b32 s69, v118, 5
	v_readlane_b32 s70, v118, 6
	v_readlane_b32 s71, v118, 7
	v_readlane_b32 s72, v118, 8
	v_readlane_b32 s73, v118, 9
	v_readlane_b32 s74, v118, 10
	v_readlane_b32 s75, v118, 11
	v_readlane_b32 s76, v118, 12
	v_readlane_b32 s77, v118, 13
	v_readlane_b32 s78, v118, 14
	v_readlane_b32 s79, v118, 15
	v_readlane_b32 s80, v118, 16
	v_readlane_b32 s81, v118, 17
	v_readlane_b32 s82, v118, 18
	v_readlane_b32 s83, v118, 19
	v_readlane_b32 s84, v118, 20
	v_readlane_b32 s85, v118, 21
	v_readlane_b32 s86, v118, 22
	v_readlane_b32 s87, v118, 23
	v_readlane_b32 s88, v118, 24
	v_readlane_b32 s89, v118, 25
	v_readlane_b32 s90, v118, 26
	v_readlane_b32 s91, v118, 27
	v_readlane_b32 s92, v118, 28
	v_readlane_b32 s93, v118, 29
	v_readlane_b32 s94, v118, 30
	v_readlane_b32 s95, v118, 31
	v_readlane_b32 s96, v118, 32
	v_readlane_b32 s97, v118, 33
	s_nop 4

	.amdhsa_kernel _Z9mixer_fwd4Args
		.amdhsa_group_segment_fixed_size 0
		.amdhsa_private_segment_fixed_size 0
		.amdhsa_kernarg_size 480
		.amdhsa_user_sgpr_count 2
		.amdhsa_user_sgpr_dispatch_ptr 0
		.amdhsa_user_sgpr_queue_ptr 0
		.amdhsa_user_sgpr_kernarg_segment_ptr 1
		.amdhsa_user_sgpr_dispatch_id 0
		.amdhsa_user_sgpr_kernarg_preload_length 0
		.amdhsa_user_sgpr_kernarg_preload_offset 0
		.amdhsa_user_sgpr_private_segment_size 0
		.amdhsa_uses_dynamic_stack 0
		.amdhsa_enable_private_segment 0
		.amdhsa_system_sgpr_workgroup_id_x 1
		.amdhsa_system_sgpr_workgroup_id_y 0
		.amdhsa_system_sgpr_workgroup_id_z 0
		.amdhsa_system_sgpr_workgroup_info 0
		.amdhsa_system_vgpr_workitem_id 0
		.amdhsa_next_free_vgpr 256
		.amdhsa_next_free_sgpr 102
		.amdhsa_accum_offset 256
		.amdhsa_reserve_vcc 1
		.amdhsa_float_round_mode_32 0
		.amdhsa_float_round_mode_16_64 0
		.amdhsa_float_denorm_mode_32 3
		.amdhsa_float_denorm_mode_16_64 3
		.amdhsa_dx10_clamp 1
		.amdhsa_ieee_mode 1
		.amdhsa_fp16_overflow 0
		.amdhsa_tg_split 0
		.amdhsa_exception_fp_ieee_invalid_op 0
		.amdhsa_exception_fp_denorm_src 0
		.amdhsa_exception_fp_ieee_div_zero 0
		.amdhsa_exception_fp_ieee_overflow 0
		.amdhsa_exception_fp_ieee_underflow 0
		.amdhsa_exception_fp_ieee_inexact 0
		.amdhsa_exception_int_div_zero 0
	.end_amdhsa_kernel

amdhsa.kernels:
  - .agpr_count:     0
    .args:
      - .offset:         0
        .size:           224
        .value_kind:     by_value
      - .offset:         224
        .size:           4
        .value_kind:     hidden_block_count_x
      - .offset:         228
        .size:           4
        .value_kind:     hidden_block_count_y
      - .offset:         232
        .size:           4
        .value_kind:     hidden_block_count_z
      - .offset:         236
        .size:           2
        .value_kind:     hidden_group_size_x
      - .offset:         238
        .size:           2
        .value_kind:     hidden_group_size_y
      - .offset:         240
        .size:           2
        .value_kind:     hidden_group_size_z
      - .offset:         242
        .size:           2
        .value_kind:     hidden_remainder_x
      - .offset:         244
        .size:           2
        .value_kind:     hidden_remainder_y
      - .offset:         246
        .size:           2
        .value_kind:     hidden_remainder_z
      - .offset:         264
        .size:           8
        .value_kind:     hidden_global_offset_x
      - .offset:         272
        .size:           8
        .value_kind:     hidden_global_offset_y
      - .offset:         280
        .size:           8
        .value_kind:     hidden_global_offset_z
      - .offset:         288
        .size:           2
        .value_kind:     hidden_grid_dims
      - .offset:         344
        .size:           4
        .value_kind:     hidden_dynamic_lds_size
    .group_segment_fixed_size: 0
    .kernarg_segment_align: 8
    .kernarg_segment_size: 480
    .language:       OpenCL C
    .language_version:
      - 2
      - 0
    .max_flat_workgroup_size: 512
    .name:           _Z9mixer_fwd4Args
    .private_segment_fixed_size: 0
    .sgpr_count:     108
    .sgpr_spill_count: 354
    .symbol:         _Z9mixer_fwd4Args.kd
    .uniform_work_group_size: 1
    .uses_dynamic_stack: false
    .vgpr_count:     256
    .vgpr_spill_count: 0
    .wavefront_size: 64
